# v73 + pool_sums: alternate window sums accumulate in v232, pairs converted with one v_cvt_pk_bf16_f32 and stored with ds_write_b16 + d16_hi (128 pairs)
# baseline (speedup 1.0000x reference)
.LBB0_583:
	s_or_b64 exec, exec, s[8:9]
	s_waitcnt lgkmcnt(0)
	s_barrier
	s_load_dwordx2 s[100:101], s[0:1], 0xd0
	v_and_b32_e32 v232, 31, v234
	v_or_b32_e32 v232, s67, v232
	v_mov_b32_e32 v233, 0
	v_lshlrev_b64 v[232:233], 8, v[232:233]
	v_lshrrev_b32_e32 v248, 5, v234
	v_and_b32_e32 v248, 1, v248
	v_lshlrev_b32_e32 v248, 4, v248
	v_mov_b32_e32 v249, 0
	v_lshl_add_u64 v[232:233], v[232:233], 0, v[248:249]
	s_waitcnt lgkmcnt(0)
	v_lshl_add_u64 v[232:233], s[100:101], 0, v[232:233]
	s_mov_b32 s100, 0x1600000
	s_mov_b32 s101, 0
	v_lshl_add_u64 v[248:249], v[232:233], 0, s[100:101]
	s_mov_b32 s100, 0x1602000
	v_lshl_add_u64 v[250:251], v[232:233], 0, s[100:101]
	global_load_dwordx4 v[168:171], v[248:249], off
	global_load_dwordx4 v[172:175], v[250:251], off
	global_load_dwordx4 v[176:179], v[248:249], off offset:32
	global_load_dwordx4 v[180:183], v[250:251], off offset:32
	global_load_dwordx4 v[184:187], v[248:249], off offset:64
	global_load_dwordx4 v[188:191], v[250:251], off offset:64
	global_load_dwordx4 v[192:195], v[248:249], off offset:96
	global_load_dwordx4 v[196:199], v[250:251], off offset:96
	global_load_dwordx4 v[200:203], v[248:249], off offset:128
	global_load_dwordx4 v[204:207], v[250:251], off offset:128
	global_load_dwordx4 v[208:211], v[248:249], off offset:160
	global_load_dwordx4 v[212:215], v[250:251], off offset:160
	global_load_dwordx4 v[216:219], v[248:249], off offset:192
	global_load_dwordx4 v[220:223], v[250:251], off offset:192
	global_load_dwordx4 v[224:227], v[248:249], off offset:224
	global_load_dwordx4 v[228:231], v[250:251], off offset:224
	v_mbcnt_lo_u32_b32 v0, -1, 0
	v_mbcnt_hi_u32_b32 v0, -1, v0
	s_and_b32 s5, s34, 31
	v_add_u32_e32 v114, s67, v0
	s_cmp_eq_u32 s5, 0
	v_lshl_add_u32 v0, v114, 1, 0
	ds_read_u16 v2, v0 offset:14560
	ds_read_u16 v3, v0 offset:15600
	ds_read_u16 v4, v0 offset:16640
	ds_read_u16 v5, v0 offset:17680
	ds_read_u16 v6, v0 offset:18720
	ds_read_u16 v7, v0 offset:19760
	ds_read_u16 v8, v0 offset:20800
	ds_read_u16 v9, v0 offset:21840
	s_waitcnt lgkmcnt(7)
	v_lshlrev_b32_e32 v115, 16, v2
	s_waitcnt lgkmcnt(6)
	v_lshlrev_b32_e32 v49, 16, v3
	s_waitcnt lgkmcnt(5)
	v_lshlrev_b32_e32 v46, 16, v4
	s_waitcnt lgkmcnt(4)
	v_lshlrev_b32_e32 v43, 16, v5
	s_waitcnt lgkmcnt(3)
	v_lshlrev_b32_e32 v41, 16, v6
	s_waitcnt lgkmcnt(2)
	v_lshlrev_b32_e32 v38, 16, v7
	s_waitcnt lgkmcnt(1)
	v_lshlrev_b32_e32 v35, 16, v8
	s_waitcnt lgkmcnt(0)
	v_lshlrev_b32_e32 v32, 16, v9
	ds_read_u16 v2, v0 offset:22880
	ds_read_u16 v3, v0 offset:23920
	ds_read_u16 v4, v0 offset:24960
	ds_read_u16 v5, v0 offset:26000
	ds_read_u16 v6, v0 offset:27040
	ds_read_u16 v7, v0 offset:28080
	ds_read_u16 v8, v0 offset:29120
	ds_read_u16 v9, v0 offset:30160
	s_waitcnt lgkmcnt(7)
	v_lshlrev_b32_e32 v39, 16, v2
	s_waitcnt lgkmcnt(6)
	v_lshlrev_b32_e32 v36, 16, v3
	s_waitcnt lgkmcnt(5)
	v_lshlrev_b32_e32 v33, 16, v4
	s_waitcnt lgkmcnt(4)
	v_lshlrev_b32_e32 v29, 16, v5
	s_waitcnt lgkmcnt(3)
	v_lshlrev_b32_e32 v26, 16, v6
	v_add_u32_e32 v2, 0x10400, v0
	v_add_u32_e32 v3, 0x10810, v0
	v_add_u32_e32 v4, 0x10c20, v0
	v_add_u32_e32 v5, 0x11030, v0
	v_add_u32_e32 v6, 0x11440, v0
	s_waitcnt lgkmcnt(2)
	v_lshlrev_b32_e32 v24, 16, v7
	s_waitcnt lgkmcnt(1)
	v_lshlrev_b32_e32 v22, 16, v8
	s_waitcnt lgkmcnt(0)
	v_lshlrev_b32_e32 v20, 16, v9
	v_add_u32_e32 v7, 0x11850, v0
	ds_read_u16 v8, v0 offset:31200
	ds_read_u16 v9, v0 offset:32240
	ds_read_u16 v2, v2
	ds_read_u16 v3, v3
	ds_read_u16 v4, v4
	ds_read_u16 v5, v5
	ds_read_u16 v6, v6
	ds_read_u16 v10, v7
	s_waitcnt lgkmcnt(7)
	v_lshlrev_b32_e32 v64, 16, v8
	s_waitcnt lgkmcnt(6)
	v_lshlrev_b32_e32 v62, 16, v9
	ds_read_u16 v7, v0 offset:33280
	ds_read_u16 v8, v0 offset:34320
	ds_read_u16 v9, v0 offset:35360
	ds_read_u16 v11, v0 offset:36400
	ds_read_u16 v12, v0 offset:37440
	ds_read_u16 v13, v0 offset:38480
	ds_read_u16 v14, v0 offset:39520
	ds_read_u16 v15, v0 offset:40560
	s_waitcnt lgkmcnt(7)
	v_lshlrev_b32_e32 v65, 16, v7
	s_waitcnt lgkmcnt(6)
	v_lshlrev_b32_e32 v63, 16, v8
	s_waitcnt lgkmcnt(5)
	v_lshlrev_b32_e32 v61, 16, v9
	s_waitcnt lgkmcnt(4)
	v_lshlrev_b32_e32 v60, 16, v11
	s_waitcnt lgkmcnt(3)
	v_lshlrev_b32_e32 v59, 16, v12
	s_waitcnt lgkmcnt(2)
	v_lshlrev_b32_e32 v58, 16, v13
	s_waitcnt lgkmcnt(1)
	v_lshlrev_b32_e32 v56, 16, v14
	s_waitcnt lgkmcnt(0)
	v_lshlrev_b32_e32 v54, 16, v15
	ds_read_u16 v7, v0 offset:41600
	ds_read_u16 v8, v0 offset:42640
	ds_read_u16 v9, v0 offset:43680
	ds_read_u16 v11, v0 offset:44720
	ds_read_u16 v12, v0 offset:45760
	ds_read_u16 v13, v0 offset:46800
	ds_read_u16 v14, v0 offset:47840
	ds_read_u16 v15, v0 offset:48880
	s_waitcnt lgkmcnt(7)
	v_lshlrev_b32_e32 v57, 16, v7
	s_waitcnt lgkmcnt(6)
	v_lshlrev_b32_e32 v55, 16, v8
	s_waitcnt lgkmcnt(5)
	v_lshlrev_b32_e32 v53, 16, v9
	s_waitcnt lgkmcnt(4)
	v_lshlrev_b32_e32 v52, 16, v11
	s_waitcnt lgkmcnt(3)
	v_lshlrev_b32_e32 v51, 16, v12
	s_waitcnt lgkmcnt(2)
	v_lshlrev_b32_e32 v50, 16, v13
	s_waitcnt lgkmcnt(1)
	v_lshlrev_b32_e32 v47, 16, v14
	s_waitcnt lgkmcnt(0)
	v_lshlrev_b32_e32 v44, 16, v15
	ds_read_u16 v7, v0 offset:49920
	ds_read_u16 v8, v0 offset:50960
	ds_read_u16 v9, v0 offset:52000
	ds_read_u16 v11, v0 offset:53040
	ds_read_u16 v12, v0 offset:54080
	ds_read_u16 v13, v0 offset:55120
	ds_read_u16 v14, v0 offset:56160
	ds_read_u16 v15, v0 offset:57200
	s_waitcnt lgkmcnt(7)
	v_lshlrev_b32_e32 v48, 16, v7
	s_waitcnt lgkmcnt(6)
	v_lshlrev_b32_e32 v45, 16, v8
	s_waitcnt lgkmcnt(5)
	v_lshlrev_b32_e32 v42, 16, v9
	s_waitcnt lgkmcnt(4)
	v_lshlrev_b32_e32 v40, 16, v11
	s_waitcnt lgkmcnt(3)
	v_lshlrev_b32_e32 v37, 16, v12
	s_waitcnt lgkmcnt(2)
	v_lshlrev_b32_e32 v34, 16, v13
	s_waitcnt lgkmcnt(1)
	v_lshlrev_b32_e32 v30, 16, v14
	s_waitcnt lgkmcnt(0)
	v_lshlrev_b32_e32 v27, 16, v15
	ds_read_u16 v7, v0 offset:58240
	ds_read_u16 v8, v0 offset:59280
	ds_read_u16 v9, v0 offset:60320
	ds_read_u16 v11, v0 offset:61360
	ds_read_u16 v12, v0 offset:62400
	ds_read_u16 v13, v0 offset:63440
	ds_read_u16 v14, v0 offset:64480
	ds_read_u16 v15, v0 offset:65520
	s_waitcnt lgkmcnt(7)
	v_lshlrev_b32_e32 v31, 16, v7
	s_waitcnt lgkmcnt(6)
	v_lshlrev_b32_e32 v28, 16, v8
	s_waitcnt lgkmcnt(5)
	v_lshlrev_b32_e32 v25, 16, v9
	s_waitcnt lgkmcnt(3)
	v_lshlrev_b32_e32 v21, 16, v12
	s_waitcnt lgkmcnt(1)
	v_lshlrev_b32_e32 v18, 16, v14
	v_lshlrev_b32_e32 v14, 16, v2
	v_lshlrev_b32_e32 v12, 16, v3
	v_lshlrev_b32_e32 v9, 16, v4
	v_lshlrev_b32_e32 v7, 16, v5
	v_lshlrev_b32_e32 v5, 16, v6
	v_lshlrev_b32_e32 v3, 16, v10
	v_add_u32_e32 v2, 0x11c60, v0
	v_add_u32_e32 v4, 0x12070, v0
	v_add_u32_e32 v6, 0x12480, v0
	v_add_u32_e32 v8, 0x12890, v0
	v_add_u32_e32 v10, 0x12ca0, v0
	v_lshlrev_b32_e32 v23, 16, v11
	v_lshlrev_b32_e32 v19, 16, v13
	s_waitcnt lgkmcnt(0)
	v_lshlrev_b32_e32 v16, 16, v15
	v_add_u32_e32 v11, 0x130b0, v0
	v_add_u32_e32 v13, 0x134c0, v0
	v_add_u32_e32 v15, 0x138d0, v0
	ds_read_u16 v2, v2
	ds_read_u16 v4, v4
	ds_read_u16 v6, v6
	ds_read_u16 v8, v8
	ds_read_u16 v10, v10
	ds_read_u16 v122, v11
	ds_read_u16 v123, v13
	ds_read_u16 v124, v15
	s_waitcnt lgkmcnt(7)
	v_lshlrev_b32_e32 v17, 16, v2
	v_add_u32_e32 v2, 0x13ce0, v0
	ds_read_u16 v2, v2
	v_readfirstlane_b32 s4, v114
	v_add_f32_e32 v114, 0, v49
	s_waitcnt lgkmcnt(7)
	v_lshlrev_b32_e32 v15, 16, v4
	s_waitcnt lgkmcnt(6)
	v_lshlrev_b32_e32 v13, 16, v6
	s_waitcnt lgkmcnt(5)
	v_lshlrev_b32_e32 v11, 16, v8
	s_waitcnt lgkmcnt(4)
	v_lshlrev_b32_e32 v10, 16, v10
	s_waitcnt lgkmcnt(3)
	v_lshlrev_b32_e32 v8, 16, v122
	s_waitcnt lgkmcnt(2)
	v_lshlrev_b32_e32 v6, 16, v123
	s_waitcnt lgkmcnt(1)
	v_lshlrev_b32_e32 v4, 16, v124
	s_waitcnt lgkmcnt(0)
	v_lshlrev_b32_e32 v2, 16, v2
	s_cselect_b64 s[6:7], -1, 0
	s_mov_b64 s[8:9], -1
	s_cmpk_gt_u32 s4, 0x7f
	v_add_f32_e32 v114, v114, v115
	s_cbranch_scc0 .LBB0_595
	ds_read_u16 v129, v0
	ds_read_u16 v130, v0 offset:1040
	ds_read_u16 v131, v0 offset:2080
	ds_read_u16 v132, v0 offset:3120
	ds_read_u16 v133, v0 offset:4160
	ds_read_u16 v134, v0 offset:5200
	ds_read_u16 v135, v0 offset:6240
	ds_read_u16 v136, v0 offset:7280
	ds_read_u16 v122, v0 offset:12480
	ds_read_u16 v123, v0 offset:13520
	ds_read_u16 v125, v0 offset:8320
	ds_read_u16 v126, v0 offset:9360
	ds_read_u16 v137, v0 offset:10400
	ds_read_u16 v138, v0 offset:11440
	s_waitcnt lgkmcnt(5)
	v_lshlrev_b32_e32 v124, 16, v122
	s_waitcnt lgkmcnt(4)
	v_lshlrev_b32_e32 v122, 16, v123
	s_ashr_i32 s14, s4, 7
	v_add_f32_e32 v123, v114, v122
	v_add_f32_e32 v123, v123, v124
	s_waitcnt lgkmcnt(3)
	v_lshlrev_b32_e32 v128, 16, v125
	s_waitcnt lgkmcnt(2)
	v_lshlrev_b32_e32 v127, 16, v126
	s_waitcnt lgkmcnt(1)
	v_lshlrev_b32_e32 v126, 16, v137
	s_waitcnt lgkmcnt(0)
	v_lshlrev_b32_e32 v125, 16, v138
	s_mov_b64 s[12:13], -1
	s_mov_b64 s[8:9], 0
	s_cmp_lt_i32 s14, 2
	s_mov_b64 s[10:11], 0
	s_cbranch_scc1 .LBB0_590
	s_cmp_eq_u32 s14, 2
	s_mov_b64 s[10:11], -1
	s_cbranch_scc0 .LBB0_587
	v_add_f32_e32 v137, v123, v125
	v_add_f32_e32 v137, v137, v126
	v_add_f32_e32 v137, v137, v127
	v_mov_b32_e32 v139, 0x3e000000
	v_add_f32_e32 v137, v137, v128
	v_cndmask_b32_e64 v138, v139, 1.0, s[6:7]
	v_fma_f32 v137, v138, v137, -v49
	v_add_f32_e32 v232, 0, v46
	v_add_f32_e32 v232, v232, v49
	v_add_f32_e32 v232, v232, v115
	v_add_f32_e32 v232, v232, v122
	v_add_f32_e32 v232, v232, v124
	v_add_f32_e32 v232, v232, v125
	v_add_f32_e32 v232, v232, v126
	v_add_f32_e32 v232, v232, v127
	v_cndmask_b32_e64 v138, v139, 0.5, s[6:7]
	v_fma_f32 v232, v138, v232, -v46
	v_cvt_pk_bf16_f32 v137, v137, v232
	ds_write_b16 v0, v137
	ds_write_b16_d16_hi v0, v137 offset:1040
	v_add_f32_e32 v137, 0, v43
	v_add_f32_e32 v137, v137, v46
	v_add_f32_e32 v137, v137, v49
	v_add_f32_e32 v137, v137, v115
	v_add_f32_e32 v137, v137, v122
	v_add_f32_e32 v137, v137, v124
	v_add_f32_e32 v137, v137, v125
	v_mov_b32_e32 v138, 0x3eaaaaab
	v_add_f32_e32 v137, v137, v126
	v_cndmask_b32_e64 v138, v139, v138, s[6:7]
	v_fma_f32 v137, v138, v137, -v43
	v_add_f32_e32 v232, 0, v41
	v_add_f32_e32 v232, v232, v43
	v_add_f32_e32 v232, v232, v46
	v_add_f32_e32 v232, v232, v49
	v_add_f32_e32 v232, v232, v115
	v_add_f32_e32 v232, v232, v122
	v_add_f32_e32 v232, v232, v124
	v_mov_b32_e32 v138, 0x3e800000
	v_add_f32_e32 v232, v232, v125
	v_cndmask_b32_e64 v138, v139, v138, s[6:7]
	v_fma_f32 v232, v138, v232, -v41
	v_cvt_pk_bf16_f32 v137, v137, v232
	ds_write_b16 v0, v137 offset:2080
	ds_write_b16_d16_hi v0, v137 offset:3120
	v_add_f32_e32 v137, 0, v38
	v_add_f32_e32 v137, v137, v41
	v_add_f32_e32 v137, v137, v43
	v_add_f32_e32 v137, v137, v46
	v_add_f32_e32 v137, v137, v49
	v_add_f32_e32 v137, v137, v115
	v_add_f32_e32 v137, v137, v122
	v_mov_b32_e32 v138, 0x3e4ccccd
	v_add_f32_e32 v137, v137, v124
	v_cndmask_b32_e64 v138, v139, v138, s[6:7]
	v_fma_f32 v137, v138, v137, -v38
	v_add_f32_e32 v232, 0, v35
	v_add_f32_e32 v232, v232, v38
	v_add_f32_e32 v232, v232, v41
	v_add_f32_e32 v232, v232, v43
	v_add_f32_e32 v232, v232, v46
	v_add_f32_e32 v232, v232, v49
	v_add_f32_e32 v232, v232, v115
	v_mov_b32_e32 v138, 0x3e2aaaab
	v_add_f32_e32 v232, v232, v122
	v_cndmask_b32_e64 v138, v139, v138, s[6:7]
	v_fma_f32 v232, v138, v232, -v35
	v_cvt_pk_bf16_f32 v137, v137, v232
	ds_write_b16 v0, v137 offset:4160
	ds_write_b16_d16_hi v0, v137 offset:5200
	v_add_f32_e32 v137, 0, v32
	v_add_f32_e32 v137, v137, v35
	v_add_f32_e32 v137, v137, v38
	v_add_f32_e32 v137, v137, v41
	v_add_f32_e32 v137, v137, v43
	v_add_f32_e32 v137, v137, v46
	v_add_f32_e32 v137, v137, v49
	v_mov_b32_e32 v138, 0x3e124925
	v_add_f32_e32 v137, v137, v115
	v_cndmask_b32_e64 v138, v139, v138, s[6:7]
	v_fma_f32 v137, v138, v137, -v32
	v_add_f32_e32 v232, 0, v39
	v_add_f32_e32 v232, v232, v32
	v_add_f32_e32 v232, v232, v35
	v_add_f32_e32 v232, v232, v38
	v_add_f32_e32 v232, v232, v41
	v_add_f32_e32 v232, v232, v43
	v_add_f32_e32 v232, v232, v46
	v_add_f32_e32 v232, v232, v49
	s_mov_b32 s4, 0x3e000000
	v_fma_f32 v232, v232, s4, -v39
	v_cvt_pk_bf16_f32 v137, v137, v232
	ds_write_b16 v0, v137 offset:6240
	ds_write_b16_d16_hi v0, v137 offset:7280
	v_add_f32_e32 v137, 0, v36
	v_add_f32_e32 v137, v137, v39
	v_add_f32_e32 v137, v137, v32
	v_add_f32_e32 v137, v137, v35
	v_add_f32_e32 v137, v137, v38
	v_add_f32_e32 v137, v137, v41
	v_add_f32_e32 v137, v137, v43
	v_add_f32_e32 v137, v137, v46
	v_fma_f32 v137, v137, s4, -v36
	v_add_f32_e32 v232, 0, v33
	v_add_f32_e32 v232, v232, v36
	v_add_f32_e32 v232, v232, v39
	v_add_f32_e32 v232, v232, v32
	v_add_f32_e32 v232, v232, v35
	v_add_f32_e32 v232, v232, v38
	v_add_f32_e32 v232, v232, v41
	v_add_f32_e32 v232, v232, v43
	v_fma_f32 v232, v232, s4, -v33
	v_cvt_pk_bf16_f32 v137, v137, v232
	ds_write_b16 v0, v137 offset:8320
	ds_write_b16_d16_hi v0, v137 offset:9360
	v_add_f32_e32 v137, 0, v29
	v_add_f32_e32 v137, v137, v33
	v_add_f32_e32 v137, v137, v36
	v_add_f32_e32 v137, v137, v39
	v_add_f32_e32 v137, v137, v32
	v_add_f32_e32 v137, v137, v35
	v_add_f32_e32 v137, v137, v38
	v_add_f32_e32 v137, v137, v41
	v_fma_f32 v137, v137, s4, -v29
	v_add_f32_e32 v232, 0, v26
	v_add_f32_e32 v232, v232, v29
	v_add_f32_e32 v232, v232, v33
	v_add_f32_e32 v232, v232, v36
	v_add_f32_e32 v232, v232, v39
	v_add_f32_e32 v232, v232, v32
	v_add_f32_e32 v232, v232, v35
	v_add_f32_e32 v232, v232, v38
	v_fma_f32 v232, v232, s4, -v26
	v_cvt_pk_bf16_f32 v137, v137, v232
	ds_write_b16 v0, v137 offset:10400
	ds_write_b16_d16_hi v0, v137 offset:11440
	v_add_f32_e32 v137, 0, v24
	v_add_f32_e32 v137, v137, v26
	v_add_f32_e32 v137, v137, v29
	v_add_f32_e32 v137, v137, v33
	v_add_f32_e32 v137, v137, v36
	v_add_f32_e32 v137, v137, v39
	v_add_f32_e32 v137, v137, v32
	v_add_f32_e32 v137, v137, v35
	v_fma_f32 v137, v137, s4, -v24
	v_add_f32_e32 v232, 0, v22
	v_add_f32_e32 v232, v232, v24
	v_add_f32_e32 v232, v232, v26
	v_add_f32_e32 v232, v232, v29
	v_add_f32_e32 v232, v232, v33
	v_add_f32_e32 v232, v232, v36
	v_add_f32_e32 v232, v232, v39
	v_add_f32_e32 v232, v232, v32
	v_fma_f32 v232, v232, s4, -v22
	v_cvt_pk_bf16_f32 v137, v137, v232
	ds_write_b16 v0, v137 offset:12480
	ds_write_b16_d16_hi v0, v137 offset:13520
	v_add_f32_e32 v137, 0, v20
	v_add_f32_e32 v137, v137, v22
	v_add_f32_e32 v137, v137, v24
	v_add_f32_e32 v137, v137, v26
	v_add_f32_e32 v137, v137, v29
	v_add_f32_e32 v137, v137, v33
	v_add_f32_e32 v137, v137, v36
	v_add_f32_e32 v137, v137, v39
	v_fma_f32 v137, v137, s4, -v20
	v_add_f32_e32 v232, 0, v64
	v_add_f32_e32 v232, v232, v20
	v_add_f32_e32 v232, v232, v22
	v_add_f32_e32 v232, v232, v24
	v_add_f32_e32 v232, v232, v26
	v_add_f32_e32 v232, v232, v29
	v_add_f32_e32 v232, v232, v33
	v_add_f32_e32 v232, v232, v36
	v_fma_f32 v232, v232, s4, -v64
	v_cvt_pk_bf16_f32 v137, v137, v232
	ds_write_b16 v0, v137 offset:14560
	ds_write_b16_d16_hi v0, v137 offset:15600
	v_add_f32_e32 v137, 0, v62
	v_add_f32_e32 v137, v137, v64
	v_add_f32_e32 v137, v137, v20
	v_add_f32_e32 v137, v137, v22
	v_add_f32_e32 v137, v137, v24
	v_add_f32_e32 v137, v137, v26
	v_add_f32_e32 v137, v137, v29
	v_add_f32_e32 v137, v137, v33
	v_fma_f32 v137, v137, s4, -v62
	v_add_f32_e32 v232, 0, v65
	v_add_f32_e32 v232, v232, v62
	v_add_f32_e32 v232, v232, v64
	v_add_f32_e32 v232, v232, v20
	v_add_f32_e32 v232, v232, v22
	v_add_f32_e32 v232, v232, v24
	v_add_f32_e32 v232, v232, v26
	v_add_f32_e32 v232, v232, v29
	v_fma_f32 v232, v232, s4, -v65
	v_cvt_pk_bf16_f32 v137, v137, v232
	ds_write_b16 v0, v137 offset:16640
	ds_write_b16_d16_hi v0, v137 offset:17680
	v_add_f32_e32 v137, 0, v63
	v_add_f32_e32 v137, v137, v65
	v_add_f32_e32 v137, v137, v62
	v_add_f32_e32 v137, v137, v64
	v_add_f32_e32 v137, v137, v20
	v_add_f32_e32 v137, v137, v22
	v_add_f32_e32 v137, v137, v24
	v_add_f32_e32 v137, v137, v26
	v_fma_f32 v137, v137, s4, -v63
	v_add_f32_e32 v232, 0, v61
	v_add_f32_e32 v232, v232, v63
	v_add_f32_e32 v232, v232, v65
	v_add_f32_e32 v232, v232, v62
	v_add_f32_e32 v232, v232, v64
	v_add_f32_e32 v232, v232, v20
	v_add_f32_e32 v232, v232, v22
	v_add_f32_e32 v232, v232, v24
	v_fma_f32 v232, v232, s4, -v61
	v_cvt_pk_bf16_f32 v137, v137, v232
	ds_write_b16 v0, v137 offset:18720
	ds_write_b16_d16_hi v0, v137 offset:19760
	v_add_f32_e32 v137, 0, v60
	v_add_f32_e32 v137, v137, v61
	v_add_f32_e32 v137, v137, v63
	v_add_f32_e32 v137, v137, v65
	v_add_f32_e32 v137, v137, v62
	v_add_f32_e32 v137, v137, v64
	v_add_f32_e32 v137, v137, v20
	v_add_f32_e32 v137, v137, v22
	v_fma_f32 v137, v137, s4, -v60
	v_add_f32_e32 v232, 0, v59
	v_add_f32_e32 v232, v232, v60
	v_add_f32_e32 v232, v232, v61
	v_add_f32_e32 v232, v232, v63
	v_add_f32_e32 v232, v232, v65
	v_add_f32_e32 v232, v232, v62
	v_add_f32_e32 v232, v232, v64
	v_add_f32_e32 v232, v232, v20
	v_fma_f32 v232, v232, s4, -v59
	v_cvt_pk_bf16_f32 v137, v137, v232
	ds_write_b16 v0, v137 offset:20800
	ds_write_b16_d16_hi v0, v137 offset:21840
	v_add_f32_e32 v137, 0, v58
	v_add_f32_e32 v137, v137, v59
	v_add_f32_e32 v137, v137, v60
	v_add_f32_e32 v137, v137, v61
	v_add_f32_e32 v137, v137, v63
	v_add_f32_e32 v137, v137, v65
	v_add_f32_e32 v137, v137, v62
	v_add_f32_e32 v137, v137, v64
	v_fma_f32 v137, v137, s4, -v58
	v_add_f32_e32 v232, 0, v56
	v_add_f32_e32 v232, v232, v58
	v_add_f32_e32 v232, v232, v59
	v_add_f32_e32 v232, v232, v60
	v_add_f32_e32 v232, v232, v61
	v_add_f32_e32 v232, v232, v63
	v_add_f32_e32 v232, v232, v65
	v_add_f32_e32 v232, v232, v62
	v_fma_f32 v232, v232, s4, -v56
	v_cvt_pk_bf16_f32 v137, v137, v232
	ds_write_b16 v0, v137 offset:22880
	ds_write_b16_d16_hi v0, v137 offset:23920
	v_add_f32_e32 v137, 0, v54
	v_add_f32_e32 v137, v137, v56
	v_add_f32_e32 v137, v137, v58
	v_add_f32_e32 v137, v137, v59
	v_add_f32_e32 v137, v137, v60
	v_add_f32_e32 v137, v137, v61
	v_add_f32_e32 v137, v137, v63
	v_add_f32_e32 v137, v137, v65
	v_fma_f32 v137, v137, s4, -v54
	v_add_f32_e32 v232, 0, v57
	v_add_f32_e32 v232, v232, v54
	v_add_f32_e32 v232, v232, v56
	v_add_f32_e32 v232, v232, v58
	v_add_f32_e32 v232, v232, v59
	v_add_f32_e32 v232, v232, v60
	v_add_f32_e32 v232, v232, v61
	v_add_f32_e32 v232, v232, v63
	v_fma_f32 v232, v232, s4, -v57
	v_cvt_pk_bf16_f32 v137, v137, v232
	ds_write_b16 v0, v137 offset:24960
	ds_write_b16_d16_hi v0, v137 offset:26000
	v_add_f32_e32 v137, 0, v55
	v_add_f32_e32 v137, v137, v57
	v_add_f32_e32 v137, v137, v54
	v_add_f32_e32 v137, v137, v56
	v_add_f32_e32 v137, v137, v58
	v_add_f32_e32 v137, v137, v59
	v_add_f32_e32 v137, v137, v60
	v_add_f32_e32 v137, v137, v61
	v_fma_f32 v137, v137, s4, -v55
	v_add_f32_e32 v232, 0, v53
	v_add_f32_e32 v232, v232, v55
	v_add_f32_e32 v232, v232, v57
	v_add_f32_e32 v232, v232, v54
	v_add_f32_e32 v232, v232, v56
	v_add_f32_e32 v232, v232, v58
	v_add_f32_e32 v232, v232, v59
	v_add_f32_e32 v232, v232, v60
	v_fma_f32 v232, v232, s4, -v53
	v_cvt_pk_bf16_f32 v137, v137, v232
	ds_write_b16 v0, v137 offset:27040
	ds_write_b16_d16_hi v0, v137 offset:28080
	v_add_f32_e32 v137, 0, v52
	v_add_f32_e32 v137, v137, v53
	v_add_f32_e32 v137, v137, v55
	v_add_f32_e32 v137, v137, v57
	v_add_f32_e32 v137, v137, v54
	v_add_f32_e32 v137, v137, v56
	v_add_f32_e32 v137, v137, v58
	v_add_f32_e32 v137, v137, v59
	v_fma_f32 v137, v137, s4, -v52
	v_add_f32_e32 v232, 0, v51
	v_add_f32_e32 v232, v232, v52
	v_add_f32_e32 v232, v232, v53
	v_add_f32_e32 v232, v232, v55
	v_add_f32_e32 v232, v232, v57
	v_add_f32_e32 v232, v232, v54
	v_add_f32_e32 v232, v232, v56
	v_add_f32_e32 v232, v232, v58
	v_fma_f32 v232, v232, s4, -v51
	v_cvt_pk_bf16_f32 v137, v137, v232
	ds_write_b16 v0, v137 offset:29120
	ds_write_b16_d16_hi v0, v137 offset:30160
	v_add_f32_e32 v137, 0, v50
	v_add_f32_e32 v137, v137, v51
	v_add_f32_e32 v137, v137, v52
	v_add_f32_e32 v137, v137, v53
	v_add_f32_e32 v137, v137, v55
	v_add_f32_e32 v137, v137, v57
	v_add_f32_e32 v137, v137, v54
	v_add_f32_e32 v137, v137, v56
	v_fma_f32 v137, v137, s4, -v50
	v_add_f32_e32 v232, 0, v47
	v_add_f32_e32 v232, v232, v50
	v_add_f32_e32 v232, v232, v51
	v_add_f32_e32 v232, v232, v52
	v_add_f32_e32 v232, v232, v53
	v_add_f32_e32 v232, v232, v55
	v_add_f32_e32 v232, v232, v57
	v_add_f32_e32 v232, v232, v54
	v_fma_f32 v232, v232, s4, -v47
	v_cvt_pk_bf16_f32 v137, v137, v232
	ds_write_b16 v0, v137 offset:31200
	ds_write_b16_d16_hi v0, v137 offset:32240
	v_add_f32_e32 v137, 0, v44
	v_add_f32_e32 v137, v137, v47
	v_add_f32_e32 v137, v137, v50
	v_add_f32_e32 v137, v137, v51
	v_add_f32_e32 v137, v137, v52
	v_add_f32_e32 v137, v137, v53
	v_add_f32_e32 v137, v137, v55
	v_add_f32_e32 v137, v137, v57
	v_fma_f32 v137, v137, s4, -v44
	v_add_f32_e32 v232, 0, v48
	v_add_f32_e32 v232, v232, v44
	v_add_f32_e32 v232, v232, v47
	v_add_f32_e32 v232, v232, v50
	v_add_f32_e32 v232, v232, v51
	v_add_f32_e32 v232, v232, v52
	v_add_f32_e32 v232, v232, v53
	v_add_f32_e32 v232, v232, v55
	v_fma_f32 v232, v232, s4, -v48
	v_cvt_pk_bf16_f32 v137, v137, v232
	ds_write_b16 v0, v137 offset:33280
	ds_write_b16_d16_hi v0, v137 offset:34320
	v_add_f32_e32 v137, 0, v45
	v_add_f32_e32 v137, v137, v48
	v_add_f32_e32 v137, v137, v44
	v_add_f32_e32 v137, v137, v47
	v_add_f32_e32 v137, v137, v50
	v_add_f32_e32 v137, v137, v51
	v_add_f32_e32 v137, v137, v52
	v_add_f32_e32 v137, v137, v53
	v_fma_f32 v137, v137, s4, -v45
	v_add_f32_e32 v232, 0, v42
	v_add_f32_e32 v232, v232, v45
	v_add_f32_e32 v232, v232, v48
	v_add_f32_e32 v232, v232, v44
	v_add_f32_e32 v232, v232, v47
	v_add_f32_e32 v232, v232, v50
	v_add_f32_e32 v232, v232, v51
	v_add_f32_e32 v232, v232, v52
	v_fma_f32 v232, v232, s4, -v42
	v_cvt_pk_bf16_f32 v137, v137, v232
	ds_write_b16 v0, v137 offset:35360
	ds_write_b16_d16_hi v0, v137 offset:36400
	v_add_f32_e32 v137, 0, v40
	v_add_f32_e32 v137, v137, v42
	v_add_f32_e32 v137, v137, v45
	v_add_f32_e32 v137, v137, v48
	v_add_f32_e32 v137, v137, v44
	v_add_f32_e32 v137, v137, v47
	v_add_f32_e32 v137, v137, v50
	v_add_f32_e32 v137, v137, v51
	v_fma_f32 v137, v137, s4, -v40
	v_add_f32_e32 v232, 0, v37
	v_add_f32_e32 v232, v232, v40
	v_add_f32_e32 v232, v232, v42
	v_add_f32_e32 v232, v232, v45
	v_add_f32_e32 v232, v232, v48
	v_add_f32_e32 v232, v232, v44
	v_add_f32_e32 v232, v232, v47
	v_add_f32_e32 v232, v232, v50
	v_fma_f32 v232, v232, s4, -v37
	v_cvt_pk_bf16_f32 v137, v137, v232
	ds_write_b16 v0, v137 offset:37440
	ds_write_b16_d16_hi v0, v137 offset:38480
	v_add_f32_e32 v137, 0, v34
	v_add_f32_e32 v137, v137, v37
	v_add_f32_e32 v137, v137, v40
	v_add_f32_e32 v137, v137, v42
	v_add_f32_e32 v137, v137, v45
	v_add_f32_e32 v137, v137, v48
	v_add_f32_e32 v137, v137, v44
	v_add_f32_e32 v137, v137, v47
	v_fma_f32 v137, v137, s4, -v34
	v_add_f32_e32 v232, 0, v30
	v_add_f32_e32 v232, v232, v34
	v_add_f32_e32 v232, v232, v37
	v_add_f32_e32 v232, v232, v40
	v_add_f32_e32 v232, v232, v42
	v_add_f32_e32 v232, v232, v45
	v_add_f32_e32 v232, v232, v48
	v_add_f32_e32 v232, v232, v44
	v_fma_f32 v232, v232, s4, -v30
	v_cvt_pk_bf16_f32 v137, v137, v232
	ds_write_b16 v0, v137 offset:39520
	ds_write_b16_d16_hi v0, v137 offset:40560
	v_add_f32_e32 v137, 0, v27
	v_add_f32_e32 v137, v137, v30
	v_add_f32_e32 v137, v137, v34
	v_add_f32_e32 v137, v137, v37
	v_add_f32_e32 v137, v137, v40
	v_add_f32_e32 v137, v137, v42
	v_add_f32_e32 v137, v137, v45
	v_add_f32_e32 v137, v137, v48
	v_fma_f32 v137, v137, s4, -v27
	v_add_f32_e32 v232, 0, v31
	v_add_f32_e32 v232, v232, v27
	v_add_f32_e32 v232, v232, v30
	v_add_f32_e32 v232, v232, v34
	v_add_f32_e32 v232, v232, v37
	v_add_f32_e32 v232, v232, v40
	v_add_f32_e32 v232, v232, v42
	v_add_f32_e32 v232, v232, v45
	v_fma_f32 v232, v232, s4, -v31
	v_cvt_pk_bf16_f32 v137, v137, v232
	ds_write_b16 v0, v137 offset:41600
	ds_write_b16_d16_hi v0, v137 offset:42640
	v_add_f32_e32 v137, 0, v28
	v_add_f32_e32 v137, v137, v31
	v_add_f32_e32 v137, v137, v27
	v_add_f32_e32 v137, v137, v30
	v_add_f32_e32 v137, v137, v34
	v_add_f32_e32 v137, v137, v37
	v_add_f32_e32 v137, v137, v40
	v_add_f32_e32 v137, v137, v42
	v_fma_f32 v137, v137, s4, -v28
	v_add_f32_e32 v232, 0, v25
	v_add_f32_e32 v232, v232, v28
	v_add_f32_e32 v232, v232, v31
	v_add_f32_e32 v232, v232, v27
	v_add_f32_e32 v232, v232, v30
	v_add_f32_e32 v232, v232, v34
	v_add_f32_e32 v232, v232, v37
	v_add_f32_e32 v232, v232, v40
	v_fma_f32 v232, v232, s4, -v25
	v_cvt_pk_bf16_f32 v137, v137, v232
	ds_write_b16 v0, v137 offset:43680
	ds_write_b16_d16_hi v0, v137 offset:44720
	v_add_f32_e32 v137, 0, v23
	v_add_f32_e32 v137, v137, v25
	v_add_f32_e32 v137, v137, v28
	v_add_f32_e32 v137, v137, v31
	v_add_f32_e32 v137, v137, v27
	v_add_f32_e32 v137, v137, v30
	v_add_f32_e32 v137, v137, v34
	v_add_f32_e32 v137, v137, v37
	v_fma_f32 v137, v137, s4, -v23
	v_add_f32_e32 v232, 0, v21
	v_add_f32_e32 v232, v232, v23
	v_add_f32_e32 v232, v232, v25
	v_add_f32_e32 v232, v232, v28
	v_add_f32_e32 v232, v232, v31
	v_add_f32_e32 v232, v232, v27
	v_add_f32_e32 v232, v232, v30
	v_add_f32_e32 v232, v232, v34
	v_fma_f32 v232, v232, s4, -v21
	v_cvt_pk_bf16_f32 v137, v137, v232
	ds_write_b16 v0, v137 offset:45760
	ds_write_b16_d16_hi v0, v137 offset:46800
	v_add_f32_e32 v137, 0, v19
	v_add_f32_e32 v137, v137, v21
	v_add_f32_e32 v137, v137, v23
	v_add_f32_e32 v137, v137, v25
	v_add_f32_e32 v137, v137, v28
	v_add_f32_e32 v137, v137, v31
	v_add_f32_e32 v137, v137, v27
	v_add_f32_e32 v137, v137, v30
	v_fma_f32 v137, v137, s4, -v19
	v_add_f32_e32 v232, 0, v18
	v_add_f32_e32 v232, v232, v19
	v_add_f32_e32 v232, v232, v21
	v_add_f32_e32 v232, v232, v23
	v_add_f32_e32 v232, v232, v25
	v_add_f32_e32 v232, v232, v28
	v_add_f32_e32 v232, v232, v31
	v_add_f32_e32 v232, v232, v27
	v_fma_f32 v232, v232, s4, -v18
	v_cvt_pk_bf16_f32 v137, v137, v232
	ds_write_b16 v0, v137 offset:47840
	ds_write_b16_d16_hi v0, v137 offset:48880
	v_add_f32_e32 v137, 0, v16
	v_add_f32_e32 v137, v137, v18
	v_add_f32_e32 v137, v137, v19
	v_add_f32_e32 v137, v137, v21
	v_add_f32_e32 v137, v137, v23
	v_add_f32_e32 v137, v137, v25
	v_add_f32_e32 v137, v137, v28
	v_add_f32_e32 v137, v137, v31
	v_fma_f32 v137, v137, s4, -v16
	v_add_f32_e32 v232, 0, v14
	v_add_f32_e32 v232, v232, v16
	v_add_f32_e32 v232, v232, v18
	v_add_f32_e32 v232, v232, v19
	v_add_f32_e32 v232, v232, v21
	v_add_f32_e32 v232, v232, v23
	v_add_f32_e32 v232, v232, v25
	v_add_f32_e32 v232, v232, v28
	v_fma_f32 v232, v232, s4, -v14
	v_cvt_pk_bf16_f32 v137, v137, v232
	ds_write_b16 v0, v137 offset:49920
	ds_write_b16_d16_hi v0, v137 offset:50960
	v_add_f32_e32 v137, 0, v12
	v_add_f32_e32 v137, v137, v14
	v_add_f32_e32 v137, v137, v16
	v_add_f32_e32 v137, v137, v18
	v_add_f32_e32 v137, v137, v19
	v_add_f32_e32 v137, v137, v21
	v_add_f32_e32 v137, v137, v23
	v_add_f32_e32 v137, v137, v25
	v_fma_f32 v137, v137, s4, -v12
	v_add_f32_e32 v232, 0, v9
	v_add_f32_e32 v232, v232, v12
	v_add_f32_e32 v232, v232, v14
	v_add_f32_e32 v232, v232, v16
	v_add_f32_e32 v232, v232, v18
	v_add_f32_e32 v232, v232, v19
	v_add_f32_e32 v232, v232, v21
	v_add_f32_e32 v232, v232, v23
	v_fma_f32 v232, v232, s4, -v9
	v_cvt_pk_bf16_f32 v137, v137, v232
	ds_write_b16 v0, v137 offset:52000
	ds_write_b16_d16_hi v0, v137 offset:53040
	v_add_f32_e32 v137, 0, v7
	v_add_f32_e32 v137, v137, v9
	v_add_f32_e32 v137, v137, v12
	v_add_f32_e32 v137, v137, v14
	v_add_f32_e32 v137, v137, v16
	v_add_f32_e32 v137, v137, v18
	v_add_f32_e32 v137, v137, v19
	v_add_f32_e32 v137, v137, v21
	v_fma_f32 v137, v137, s4, -v7
	v_add_f32_e32 v232, 0, v5
	v_add_f32_e32 v232, v232, v7
	v_add_f32_e32 v232, v232, v9
	v_add_f32_e32 v232, v232, v12
	v_add_f32_e32 v232, v232, v14
	v_add_f32_e32 v232, v232, v16
	v_add_f32_e32 v232, v232, v18
	v_add_f32_e32 v232, v232, v19
	v_fma_f32 v232, v232, s4, -v5
	v_cvt_pk_bf16_f32 v137, v137, v232
	ds_write_b16 v0, v137 offset:54080
	ds_write_b16_d16_hi v0, v137 offset:55120
	v_add_f32_e32 v137, 0, v3
	v_add_f32_e32 v137, v137, v5
	v_add_f32_e32 v137, v137, v7
	v_add_f32_e32 v137, v137, v9
	v_add_f32_e32 v137, v137, v12
	v_add_f32_e32 v137, v137, v14
	v_add_f32_e32 v137, v137, v16
	v_add_f32_e32 v137, v137, v18
	v_fma_f32 v137, v137, s4, -v3
	v_add_f32_e32 v232, 0, v17
	v_add_f32_e32 v232, v232, v3
	v_add_f32_e32 v232, v232, v5
	v_add_f32_e32 v232, v232, v7
	v_add_f32_e32 v232, v232, v9
	v_add_f32_e32 v232, v232, v12
	v_add_f32_e32 v232, v232, v14
	v_add_f32_e32 v232, v232, v16
	v_fma_f32 v232, v232, s4, -v17
	v_cvt_pk_bf16_f32 v137, v137, v232
	ds_write_b16 v0, v137 offset:56160
	ds_write_b16_d16_hi v0, v137 offset:57200
	v_add_f32_e32 v137, 0, v15
	v_add_f32_e32 v137, v137, v17
	v_add_f32_e32 v137, v137, v3
	v_add_f32_e32 v137, v137, v5
	v_add_f32_e32 v137, v137, v7
	v_add_f32_e32 v137, v137, v9
	v_add_f32_e32 v137, v137, v12
	v_add_f32_e32 v137, v137, v14
	v_fma_f32 v137, v137, s4, -v15
	v_add_f32_e32 v232, 0, v13
	v_add_f32_e32 v232, v232, v15
	v_add_f32_e32 v232, v232, v17
	v_add_f32_e32 v232, v232, v3
	v_add_f32_e32 v232, v232, v5
	v_add_f32_e32 v232, v232, v7
	v_add_f32_e32 v232, v232, v9
	v_add_f32_e32 v232, v232, v12
	v_fma_f32 v232, v232, s4, -v13
	v_cvt_pk_bf16_f32 v137, v137, v232
	ds_write_b16 v0, v137 offset:58240
	ds_write_b16_d16_hi v0, v137 offset:59280
	v_add_f32_e32 v137, 0, v11
	v_add_f32_e32 v137, v137, v13
	v_add_f32_e32 v137, v137, v15
	v_add_f32_e32 v137, v137, v17
	v_add_f32_e32 v137, v137, v3
	v_add_f32_e32 v137, v137, v5
	v_add_f32_e32 v137, v137, v7
	v_add_f32_e32 v137, v137, v9
	v_fma_f32 v137, v137, s4, -v11
	v_add_f32_e32 v232, 0, v10
	v_add_f32_e32 v232, v232, v11
	v_add_f32_e32 v232, v232, v13
	v_add_f32_e32 v232, v232, v15
	v_add_f32_e32 v232, v232, v17
	v_add_f32_e32 v232, v232, v3
	v_add_f32_e32 v232, v232, v5
	v_add_f32_e32 v232, v232, v7
	v_fma_f32 v232, v232, s4, -v10
	v_cvt_pk_bf16_f32 v137, v137, v232
	ds_write_b16 v0, v137 offset:60320
	ds_write_b16_d16_hi v0, v137 offset:61360
	v_add_f32_e32 v137, 0, v8
	v_add_f32_e32 v137, v137, v10
	v_add_f32_e32 v137, v137, v11
	v_add_f32_e32 v137, v137, v13
	v_add_f32_e32 v137, v137, v15
	v_add_f32_e32 v137, v137, v17
	v_add_f32_e32 v137, v137, v3
	v_add_f32_e32 v137, v137, v5
	v_fma_f32 v137, v137, s4, -v8
	v_add_f32_e32 v232, 0, v6
	v_add_f32_e32 v232, v232, v8
	v_add_f32_e32 v232, v232, v10
	v_add_f32_e32 v232, v232, v11
	v_add_f32_e32 v232, v232, v13
	v_add_f32_e32 v232, v232, v15
	v_add_f32_e32 v232, v232, v17
	v_add_f32_e32 v232, v232, v3
	v_fma_f32 v232, v232, s4, -v6
	v_cvt_pk_bf16_f32 v137, v137, v232
	ds_write_b16 v0, v137 offset:62400
	ds_write_b16_d16_hi v0, v137 offset:63440
	v_add_f32_e32 v137, 0, v4
	v_add_f32_e32 v137, v137, v6
	v_add_f32_e32 v137, v137, v8
	v_add_f32_e32 v137, v137, v10
	v_add_f32_e32 v137, v137, v11
	v_add_f32_e32 v137, v137, v13
	v_add_f32_e32 v137, v137, v15
	v_add_f32_e32 v137, v137, v17
	v_fma_f32 v137, v137, s4, -v4
	v_cvt_pk_bf16_f32 v137, v137, s0
	ds_write_b16 v0, v137 offset:64480
	v_add_f32_e32 v137, 0, v2
	v_add_f32_e32 v137, v137, v4
	v_add_f32_e32 v137, v137, v6
	v_add_f32_e32 v137, v137, v8
	v_add_f32_e32 v137, v137, v10
	v_add_f32_e32 v137, v137, v11
	v_add_f32_e32 v137, v137, v13
	v_add_f32_e32 v137, v137, v15
	v_mul_f32_e32 v137, 0x3e000000, v137
	s_mov_b64 s[10:11], 0

.LBB0_589:
	v_add_f32_e32 v137, v123, v125
	v_add_f32_e32 v137, v137, v126
	v_add_f32_e32 v137, v137, v127
	v_lshlrev_b32_e32 v136, 16, v136
	v_add_f32_e32 v137, v137, v128
	v_lshlrev_b32_e32 v135, 16, v135
	v_add_f32_e32 v137, v137, v136
	v_lshlrev_b32_e32 v134, 16, v134
	v_add_f32_e32 v137, v137, v135
	v_lshlrev_b32_e32 v133, 16, v133
	v_add_f32_e32 v137, v137, v134
	v_lshlrev_b32_e32 v132, 16, v132
	v_add_f32_e32 v137, v137, v133
	v_lshlrev_b32_e32 v131, 16, v131
	v_add_f32_e32 v137, v137, v132
	v_lshlrev_b32_e32 v130, 16, v130
	v_add_f32_e32 v137, v137, v131
	v_lshlrev_b32_e32 v129, 16, v129
	v_add_f32_e32 v137, v137, v130
	v_mov_b32_e32 v138, 0x3d800000
	v_add_f32_e32 v129, v137, v129
	v_cndmask_b32_e64 v137, v138, 1.0, s[6:7]
	v_fma_f32 v129, v137, v129, -v49
	v_add_f32_e32 v232, 0, v46
	v_add_f32_e32 v232, v232, v49
	v_add_f32_e32 v232, v232, v115
	v_add_f32_e32 v232, v232, v122
	v_add_f32_e32 v232, v232, v124
	v_add_f32_e32 v232, v232, v125
	v_add_f32_e32 v232, v232, v126
	v_add_f32_e32 v232, v232, v127
	v_add_f32_e32 v232, v232, v128
	v_add_f32_e32 v232, v232, v136
	v_add_f32_e32 v232, v232, v135
	v_add_f32_e32 v232, v232, v134
	v_add_f32_e32 v232, v232, v133
	v_add_f32_e32 v232, v232, v132
	v_add_f32_e32 v232, v232, v131
	v_add_f32_e32 v232, v232, v130
	v_cndmask_b32_e64 v130, v138, 0.5, s[6:7]
	v_fma_f32 v232, v130, v232, -v46
	v_cvt_pk_bf16_f32 v129, v129, v232
	ds_write_b16 v0, v129
	ds_write_b16_d16_hi v0, v129 offset:1040
	v_add_f32_e32 v129, 0, v43
	v_add_f32_e32 v129, v129, v46
	v_add_f32_e32 v129, v129, v49
	v_add_f32_e32 v129, v129, v115
	v_add_f32_e32 v129, v129, v122
	v_add_f32_e32 v129, v129, v124
	v_add_f32_e32 v129, v129, v125
	v_add_f32_e32 v129, v129, v126
	v_add_f32_e32 v129, v129, v127
	v_add_f32_e32 v129, v129, v128
	v_add_f32_e32 v129, v129, v136
	v_add_f32_e32 v129, v129, v135
	v_add_f32_e32 v129, v129, v134
	v_add_f32_e32 v129, v129, v133
	v_add_f32_e32 v129, v129, v132
	v_mov_b32_e32 v130, 0x3eaaaaab
	v_add_f32_e32 v129, v129, v131
	v_cndmask_b32_e64 v130, v138, v130, s[6:7]
	v_fma_f32 v129, v130, v129, -v43
	v_add_f32_e32 v232, 0, v41
	v_add_f32_e32 v232, v232, v43
	v_add_f32_e32 v232, v232, v46
	v_add_f32_e32 v232, v232, v49
	v_add_f32_e32 v232, v232, v115
	v_add_f32_e32 v232, v232, v122
	v_add_f32_e32 v232, v232, v124
	v_add_f32_e32 v232, v232, v125
	v_add_f32_e32 v232, v232, v126
	v_add_f32_e32 v232, v232, v127
	v_add_f32_e32 v232, v232, v128
	v_add_f32_e32 v232, v232, v136
	v_add_f32_e32 v232, v232, v135
	v_add_f32_e32 v232, v232, v134
	v_add_f32_e32 v232, v232, v133
	v_mov_b32_e32 v130, 0x3e800000
	v_add_f32_e32 v232, v232, v132
	v_cndmask_b32_e64 v130, v138, v130, s[6:7]
	v_fma_f32 v232, v130, v232, -v41
	v_cvt_pk_bf16_f32 v129, v129, v232
	ds_write_b16 v0, v129 offset:2080
	ds_write_b16_d16_hi v0, v129 offset:3120
	v_add_f32_e32 v129, 0, v38
	v_add_f32_e32 v129, v129, v41
	v_add_f32_e32 v129, v129, v43
	v_add_f32_e32 v129, v129, v46
	v_add_f32_e32 v129, v129, v49
	v_add_f32_e32 v129, v129, v115
	v_add_f32_e32 v129, v129, v122
	v_add_f32_e32 v129, v129, v124
	v_add_f32_e32 v129, v129, v125
	v_add_f32_e32 v129, v129, v126
	v_add_f32_e32 v129, v129, v127
	v_add_f32_e32 v129, v129, v128
	v_add_f32_e32 v129, v129, v136
	v_add_f32_e32 v129, v129, v135
	v_add_f32_e32 v129, v129, v134
	v_mov_b32_e32 v130, 0x3e4ccccd
	v_add_f32_e32 v129, v129, v133
	v_cndmask_b32_e64 v130, v138, v130, s[6:7]
	v_fma_f32 v129, v130, v129, -v38
	v_add_f32_e32 v232, 0, v35
	v_add_f32_e32 v232, v232, v38
	v_add_f32_e32 v232, v232, v41
	v_add_f32_e32 v232, v232, v43
	v_add_f32_e32 v232, v232, v46
	v_add_f32_e32 v232, v232, v49
	v_add_f32_e32 v232, v232, v115
	v_add_f32_e32 v232, v232, v122
	v_add_f32_e32 v232, v232, v124
	v_add_f32_e32 v232, v232, v125
	v_add_f32_e32 v232, v232, v126
	v_add_f32_e32 v232, v232, v127
	v_add_f32_e32 v232, v232, v128
	v_add_f32_e32 v232, v232, v136
	v_add_f32_e32 v232, v232, v135
	v_mov_b32_e32 v130, 0x3e2aaaab
	v_add_f32_e32 v232, v232, v134
	v_cndmask_b32_e64 v130, v138, v130, s[6:7]
	v_fma_f32 v232, v130, v232, -v35
	v_cvt_pk_bf16_f32 v129, v129, v232
	ds_write_b16 v0, v129 offset:4160
	ds_write_b16_d16_hi v0, v129 offset:5200
	v_add_f32_e32 v129, 0, v32
	v_add_f32_e32 v129, v129, v35
	v_add_f32_e32 v129, v129, v38
	v_add_f32_e32 v129, v129, v41
	v_add_f32_e32 v129, v129, v43
	v_add_f32_e32 v129, v129, v46
	v_add_f32_e32 v129, v129, v49
	v_add_f32_e32 v129, v129, v115
	v_add_f32_e32 v129, v129, v122
	v_add_f32_e32 v129, v129, v124
	v_add_f32_e32 v129, v129, v125
	v_add_f32_e32 v129, v129, v126
	v_add_f32_e32 v129, v129, v127
	v_add_f32_e32 v129, v129, v128
	v_add_f32_e32 v129, v129, v136
	v_mov_b32_e32 v130, 0x3e124925
	v_add_f32_e32 v129, v129, v135
	v_cndmask_b32_e64 v130, v138, v130, s[6:7]
	v_fma_f32 v129, v130, v129, -v32
	v_add_f32_e32 v232, 0, v39
	v_add_f32_e32 v232, v232, v32
	v_add_f32_e32 v232, v232, v35
	v_add_f32_e32 v232, v232, v38
	v_add_f32_e32 v232, v232, v41
	v_add_f32_e32 v232, v232, v43
	v_add_f32_e32 v232, v232, v46
	v_add_f32_e32 v232, v232, v49
	v_add_f32_e32 v232, v232, v115
	v_add_f32_e32 v232, v232, v122
	v_add_f32_e32 v232, v232, v124
	v_add_f32_e32 v232, v232, v125
	v_add_f32_e32 v232, v232, v126
	v_add_f32_e32 v232, v232, v127
	v_add_f32_e32 v232, v232, v128
	v_mov_b32_e32 v130, 0x3e000000
	v_add_f32_e32 v232, v232, v136
	v_cndmask_b32_e64 v130, v138, v130, s[6:7]
	v_fma_f32 v232, v130, v232, -v39
	v_cvt_pk_bf16_f32 v129, v129, v232
	ds_write_b16 v0, v129 offset:6240
	ds_write_b16_d16_hi v0, v129 offset:7280
	v_add_f32_e32 v129, 0, v36
	v_add_f32_e32 v129, v129, v39
	v_add_f32_e32 v129, v129, v32
	v_add_f32_e32 v129, v129, v35
	v_add_f32_e32 v129, v129, v38
	v_add_f32_e32 v129, v129, v41
	v_add_f32_e32 v129, v129, v43
	v_add_f32_e32 v129, v129, v46
	v_add_f32_e32 v129, v129, v49
	v_add_f32_e32 v129, v129, v115
	v_add_f32_e32 v129, v129, v122
	v_add_f32_e32 v129, v129, v124
	v_add_f32_e32 v129, v129, v125
	v_add_f32_e32 v129, v129, v126
	v_add_f32_e32 v129, v129, v127
	v_add_f32_e32 v128, v129, v128
	v_mov_b32_e32 v129, 0x3de38e39
	v_cndmask_b32_e64 v129, v138, v129, s[6:7]
	v_fma_f32 v128, v129, v128, -v36
	v_cvt_pk_bf16_f32 v128, v128, s0
	ds_write_b16 v0, v128 offset:8320
	v_add_f32_e32 v128, 0, v33
	v_add_f32_e32 v128, v128, v36
	v_add_f32_e32 v128, v128, v39
	v_add_f32_e32 v128, v128, v32
	v_add_f32_e32 v128, v128, v35
	v_add_f32_e32 v128, v128, v38
	v_add_f32_e32 v128, v128, v41
	v_add_f32_e32 v128, v128, v43
	v_add_f32_e32 v128, v128, v46
	v_add_f32_e32 v128, v128, v49
	v_add_f32_e32 v128, v128, v115
	v_add_f32_e32 v128, v128, v122
	v_add_f32_e32 v128, v128, v124
	v_add_f32_e32 v128, v128, v125
	v_add_f32_e32 v128, v128, v126
	v_add_f32_e32 v127, v128, v127
	v_mov_b32_e32 v128, 0x3dcccccd
	v_cndmask_b32_e64 v128, v138, v128, s[6:7]
	v_fma_f32 v127, v128, v127, -v33
	v_cvt_pk_bf16_f32 v127, v127, s0
	ds_write_b16 v0, v127 offset:9360
	v_add_f32_e32 v127, 0, v29
	v_add_f32_e32 v127, v127, v33
	v_add_f32_e32 v127, v127, v36
	v_add_f32_e32 v127, v127, v39
	v_add_f32_e32 v127, v127, v32
	v_add_f32_e32 v127, v127, v35
	v_add_f32_e32 v127, v127, v38
	v_add_f32_e32 v127, v127, v41
	v_add_f32_e32 v127, v127, v43
	v_add_f32_e32 v127, v127, v46
	v_add_f32_e32 v127, v127, v49
	v_add_f32_e32 v127, v127, v115
	v_add_f32_e32 v127, v127, v122
	v_add_f32_e32 v127, v127, v124
	v_add_f32_e32 v127, v127, v125
	v_add_f32_e32 v126, v127, v126
	v_mov_b32_e32 v127, 0x3dba2e8c
	v_cndmask_b32_e64 v127, v138, v127, s[6:7]
	v_fma_f32 v126, v127, v126, -v29
	v_cvt_pk_bf16_f32 v126, v126, s0
	ds_write_b16 v0, v126 offset:10400
	v_add_f32_e32 v126, 0, v26
	v_add_f32_e32 v126, v126, v29
	v_add_f32_e32 v126, v126, v33
	v_add_f32_e32 v126, v126, v36
	v_add_f32_e32 v126, v126, v39
	v_add_f32_e32 v126, v126, v32
	v_add_f32_e32 v126, v126, v35
	v_add_f32_e32 v126, v126, v38
	v_add_f32_e32 v126, v126, v41
	v_add_f32_e32 v126, v126, v43
	v_add_f32_e32 v126, v126, v46
	v_add_f32_e32 v126, v126, v49
	v_add_f32_e32 v126, v126, v115
	v_add_f32_e32 v126, v126, v122
	v_add_f32_e32 v126, v126, v124
	v_add_f32_e32 v125, v126, v125
	v_mov_b32_e32 v126, 0x3daaaaab
	v_cndmask_b32_e64 v126, v138, v126, s[6:7]
	v_fma_f32 v125, v126, v125, -v26
	v_cvt_pk_bf16_f32 v125, v125, s0
	ds_write_b16 v0, v125 offset:11440
	v_add_f32_e32 v125, 0, v24
	v_add_f32_e32 v125, v125, v26
	v_add_f32_e32 v125, v125, v29
	v_add_f32_e32 v125, v125, v33
	v_add_f32_e32 v125, v125, v36
	v_add_f32_e32 v125, v125, v39
	v_add_f32_e32 v125, v125, v32
	v_add_f32_e32 v125, v125, v35
	v_add_f32_e32 v125, v125, v38
	v_add_f32_e32 v125, v125, v41
	v_add_f32_e32 v125, v125, v43
	v_add_f32_e32 v125, v125, v46
	v_add_f32_e32 v125, v125, v49
	v_add_f32_e32 v125, v125, v115
	v_add_f32_e32 v125, v125, v122
	v_add_f32_e32 v124, v125, v124
	v_mov_b32_e32 v125, 0x3d9d89d9
	v_cndmask_b32_e64 v125, v138, v125, s[6:7]
	v_fma_f32 v124, v125, v124, -v24
	v_add_f32_e32 v232, 0, v22
	v_add_f32_e32 v232, v232, v24
	v_add_f32_e32 v232, v232, v26
	v_add_f32_e32 v232, v232, v29
	v_add_f32_e32 v232, v232, v33
	v_add_f32_e32 v232, v232, v36
	v_add_f32_e32 v232, v232, v39
	v_add_f32_e32 v232, v232, v32
	v_add_f32_e32 v232, v232, v35
	v_add_f32_e32 v232, v232, v38
	v_add_f32_e32 v232, v232, v41
	v_add_f32_e32 v232, v232, v43
	v_add_f32_e32 v232, v232, v46
	v_add_f32_e32 v232, v232, v49
	v_add_f32_e32 v232, v232, v115
	v_mov_b32_e32 v125, 0x3d924925
	v_add_f32_e32 v232, v232, v122
	v_cndmask_b32_e64 v125, v138, v125, s[6:7]
	v_fma_f32 v232, v125, v232, -v22
	v_cvt_pk_bf16_f32 v124, v124, v232
	ds_write_b16 v0, v124 offset:12480
	ds_write_b16_d16_hi v0, v124 offset:13520
	v_add_f32_e32 v124, 0, v20
	v_add_f32_e32 v124, v124, v22
	v_add_f32_e32 v124, v124, v24
	v_add_f32_e32 v124, v124, v26
	v_add_f32_e32 v124, v124, v29
	v_add_f32_e32 v124, v124, v33
	v_add_f32_e32 v124, v124, v36
	v_add_f32_e32 v124, v124, v39
	v_add_f32_e32 v124, v124, v32
	v_add_f32_e32 v124, v124, v35
	v_add_f32_e32 v124, v124, v38
	v_add_f32_e32 v124, v124, v41
	v_add_f32_e32 v124, v124, v43
	v_add_f32_e32 v124, v124, v46
	v_add_f32_e32 v124, v124, v49
	v_mov_b32_e32 v125, 0x3d888889
	v_add_f32_e32 v124, v124, v115
	v_cndmask_b32_e64 v125, v138, v125, s[6:7]
	v_fma_f32 v124, v125, v124, -v20
	v_add_f32_e32 v232, 0, v64
	v_add_f32_e32 v232, v232, v20
	v_add_f32_e32 v232, v232, v22
	v_add_f32_e32 v232, v232, v24
	v_add_f32_e32 v232, v232, v26
	v_add_f32_e32 v232, v232, v29
	v_add_f32_e32 v232, v232, v33
	v_add_f32_e32 v232, v232, v36
	v_add_f32_e32 v232, v232, v39
	v_add_f32_e32 v232, v232, v32
	v_add_f32_e32 v232, v232, v35
	v_add_f32_e32 v232, v232, v38
	v_add_f32_e32 v232, v232, v41
	v_add_f32_e32 v232, v232, v43
	v_add_f32_e32 v232, v232, v46
	v_add_f32_e32 v232, v232, v49
	s_mov_b32 s4, 0x3d800000
	v_fma_f32 v232, v232, s4, -v64
	v_cvt_pk_bf16_f32 v124, v124, v232
	ds_write_b16 v0, v124 offset:14560
	ds_write_b16_d16_hi v0, v124 offset:15600
	v_add_f32_e32 v124, 0, v62
	v_add_f32_e32 v124, v124, v64
	v_add_f32_e32 v124, v124, v20
	v_add_f32_e32 v124, v124, v22
	v_add_f32_e32 v124, v124, v24
	v_add_f32_e32 v124, v124, v26
	v_add_f32_e32 v124, v124, v29
	v_add_f32_e32 v124, v124, v33
	v_add_f32_e32 v124, v124, v36
	v_add_f32_e32 v124, v124, v39
	v_add_f32_e32 v124, v124, v32
	v_add_f32_e32 v124, v124, v35
	v_add_f32_e32 v124, v124, v38
	v_add_f32_e32 v124, v124, v41
	v_add_f32_e32 v124, v124, v43
	v_add_f32_e32 v124, v124, v46
	v_fma_f32 v124, v124, s4, -v62
	v_add_f32_e32 v232, 0, v65
	v_add_f32_e32 v232, v232, v62
	v_add_f32_e32 v232, v232, v64
	v_add_f32_e32 v232, v232, v20
	v_add_f32_e32 v232, v232, v22
	v_add_f32_e32 v232, v232, v24
	v_add_f32_e32 v232, v232, v26
	v_add_f32_e32 v232, v232, v29
	v_add_f32_e32 v232, v232, v33
	v_add_f32_e32 v232, v232, v36
	v_add_f32_e32 v232, v232, v39
	v_add_f32_e32 v232, v232, v32
	v_add_f32_e32 v232, v232, v35
	v_add_f32_e32 v232, v232, v38
	v_add_f32_e32 v232, v232, v41
	v_add_f32_e32 v232, v232, v43
	v_fma_f32 v232, v232, s4, -v65
	v_cvt_pk_bf16_f32 v124, v124, v232
	ds_write_b16 v0, v124 offset:16640
	ds_write_b16_d16_hi v0, v124 offset:17680
	v_add_f32_e32 v124, 0, v63
	v_add_f32_e32 v124, v124, v65
	v_add_f32_e32 v124, v124, v62
	v_add_f32_e32 v124, v124, v64
	v_add_f32_e32 v124, v124, v20
	v_add_f32_e32 v124, v124, v22
	v_add_f32_e32 v124, v124, v24
	v_add_f32_e32 v124, v124, v26
	v_add_f32_e32 v124, v124, v29
	v_add_f32_e32 v124, v124, v33
	v_add_f32_e32 v124, v124, v36
	v_add_f32_e32 v124, v124, v39
	v_add_f32_e32 v124, v124, v32
	v_add_f32_e32 v124, v124, v35
	v_add_f32_e32 v124, v124, v38
	v_add_f32_e32 v124, v124, v41
	v_fma_f32 v124, v124, s4, -v63
	v_add_f32_e32 v232, 0, v61
	v_add_f32_e32 v232, v232, v63
	v_add_f32_e32 v232, v232, v65
	v_add_f32_e32 v232, v232, v62
	v_add_f32_e32 v232, v232, v64
	v_add_f32_e32 v232, v232, v20
	v_add_f32_e32 v232, v232, v22
	v_add_f32_e32 v232, v232, v24
	v_add_f32_e32 v232, v232, v26
	v_add_f32_e32 v232, v232, v29
	v_add_f32_e32 v232, v232, v33
	v_add_f32_e32 v232, v232, v36
	v_add_f32_e32 v232, v232, v39
	v_add_f32_e32 v232, v232, v32
	v_add_f32_e32 v232, v232, v35
	v_add_f32_e32 v232, v232, v38
	v_fma_f32 v232, v232, s4, -v61
	v_cvt_pk_bf16_f32 v124, v124, v232
	ds_write_b16 v0, v124 offset:18720
	ds_write_b16_d16_hi v0, v124 offset:19760
	v_add_f32_e32 v124, 0, v60
	v_add_f32_e32 v124, v124, v61
	v_add_f32_e32 v124, v124, v63
	v_add_f32_e32 v124, v124, v65
	v_add_f32_e32 v124, v124, v62
	v_add_f32_e32 v124, v124, v64
	v_add_f32_e32 v124, v124, v20
	v_add_f32_e32 v124, v124, v22
	v_add_f32_e32 v124, v124, v24
	v_add_f32_e32 v124, v124, v26
	v_add_f32_e32 v124, v124, v29
	v_add_f32_e32 v124, v124, v33
	v_add_f32_e32 v124, v124, v36
	v_add_f32_e32 v124, v124, v39
	v_add_f32_e32 v124, v124, v32
	v_add_f32_e32 v124, v124, v35
	v_fma_f32 v124, v124, s4, -v60
	v_add_f32_e32 v232, 0, v59
	v_add_f32_e32 v232, v232, v60
	v_add_f32_e32 v232, v232, v61
	v_add_f32_e32 v232, v232, v63
	v_add_f32_e32 v232, v232, v65
	v_add_f32_e32 v232, v232, v62
	v_add_f32_e32 v232, v232, v64
	v_add_f32_e32 v232, v232, v20
	v_add_f32_e32 v232, v232, v22
	v_add_f32_e32 v232, v232, v24
	v_add_f32_e32 v232, v232, v26
	v_add_f32_e32 v232, v232, v29
	v_add_f32_e32 v232, v232, v33
	v_add_f32_e32 v232, v232, v36
	v_add_f32_e32 v232, v232, v39
	v_add_f32_e32 v232, v232, v32
	v_fma_f32 v232, v232, s4, -v59
	v_cvt_pk_bf16_f32 v124, v124, v232
	ds_write_b16 v0, v124 offset:20800
	ds_write_b16_d16_hi v0, v124 offset:21840
	v_add_f32_e32 v124, 0, v58
	v_add_f32_e32 v124, v124, v59
	v_add_f32_e32 v124, v124, v60
	v_add_f32_e32 v124, v124, v61
	v_add_f32_e32 v124, v124, v63
	v_add_f32_e32 v124, v124, v65
	v_add_f32_e32 v124, v124, v62
	v_add_f32_e32 v124, v124, v64
	v_add_f32_e32 v124, v124, v20
	v_add_f32_e32 v124, v124, v22
	v_add_f32_e32 v124, v124, v24
	v_add_f32_e32 v124, v124, v26
	v_add_f32_e32 v124, v124, v29
	v_add_f32_e32 v124, v124, v33
	v_add_f32_e32 v124, v124, v36
	v_add_f32_e32 v124, v124, v39
	v_fma_f32 v124, v124, s4, -v58
	v_add_f32_e32 v232, 0, v56
	v_add_f32_e32 v232, v232, v58
	v_add_f32_e32 v232, v232, v59
	v_add_f32_e32 v232, v232, v60
	v_add_f32_e32 v232, v232, v61
	v_add_f32_e32 v232, v232, v63
	v_add_f32_e32 v232, v232, v65
	v_add_f32_e32 v232, v232, v62
	v_add_f32_e32 v232, v232, v64
	v_add_f32_e32 v232, v232, v20
	v_add_f32_e32 v232, v232, v22
	v_add_f32_e32 v232, v232, v24
	v_add_f32_e32 v232, v232, v26
	v_add_f32_e32 v232, v232, v29
	v_add_f32_e32 v232, v232, v33
	v_add_f32_e32 v232, v232, v36
	v_fma_f32 v232, v232, s4, -v56
	v_cvt_pk_bf16_f32 v124, v124, v232
	ds_write_b16 v0, v124 offset:22880
	ds_write_b16_d16_hi v0, v124 offset:23920
	v_add_f32_e32 v124, 0, v54
	v_add_f32_e32 v124, v124, v56
	v_add_f32_e32 v124, v124, v58
	v_add_f32_e32 v124, v124, v59
	v_add_f32_e32 v124, v124, v60
	v_add_f32_e32 v124, v124, v61
	v_add_f32_e32 v124, v124, v63
	v_add_f32_e32 v124, v124, v65
	v_add_f32_e32 v124, v124, v62
	v_add_f32_e32 v124, v124, v64
	v_add_f32_e32 v124, v124, v20
	v_add_f32_e32 v124, v124, v22
	v_add_f32_e32 v124, v124, v24
	v_add_f32_e32 v124, v124, v26
	v_add_f32_e32 v124, v124, v29
	v_add_f32_e32 v124, v124, v33
	v_fma_f32 v124, v124, s4, -v54
	v_add_f32_e32 v232, 0, v57
	v_add_f32_e32 v232, v232, v54
	v_add_f32_e32 v232, v232, v56
	v_add_f32_e32 v232, v232, v58
	v_add_f32_e32 v232, v232, v59
	v_add_f32_e32 v232, v232, v60
	v_add_f32_e32 v232, v232, v61
	v_add_f32_e32 v232, v232, v63
	v_add_f32_e32 v232, v232, v65
	v_add_f32_e32 v232, v232, v62
	v_add_f32_e32 v232, v232, v64
	v_add_f32_e32 v232, v232, v20
	v_add_f32_e32 v232, v232, v22
	v_add_f32_e32 v232, v232, v24
	v_add_f32_e32 v232, v232, v26
	v_add_f32_e32 v232, v232, v29
	v_fma_f32 v232, v232, s4, -v57
	v_cvt_pk_bf16_f32 v124, v124, v232
	ds_write_b16 v0, v124 offset:24960
	ds_write_b16_d16_hi v0, v124 offset:26000
	v_add_f32_e32 v124, 0, v55
	v_add_f32_e32 v124, v124, v57
	v_add_f32_e32 v124, v124, v54
	v_add_f32_e32 v124, v124, v56
	v_add_f32_e32 v124, v124, v58
	v_add_f32_e32 v124, v124, v59
	v_add_f32_e32 v124, v124, v60
	v_add_f32_e32 v124, v124, v61
	v_add_f32_e32 v124, v124, v63
	v_add_f32_e32 v124, v124, v65
	v_add_f32_e32 v124, v124, v62
	v_add_f32_e32 v124, v124, v64
	v_add_f32_e32 v124, v124, v20
	v_add_f32_e32 v124, v124, v22
	v_add_f32_e32 v124, v124, v24
	v_add_f32_e32 v124, v124, v26
	v_fma_f32 v124, v124, s4, -v55
	v_add_f32_e32 v232, 0, v53
	v_add_f32_e32 v232, v232, v55
	v_add_f32_e32 v232, v232, v57
	v_add_f32_e32 v232, v232, v54
	v_add_f32_e32 v232, v232, v56
	v_add_f32_e32 v232, v232, v58
	v_add_f32_e32 v232, v232, v59
	v_add_f32_e32 v232, v232, v60
	v_add_f32_e32 v232, v232, v61
	v_add_f32_e32 v232, v232, v63
	v_add_f32_e32 v232, v232, v65
	v_add_f32_e32 v232, v232, v62
	v_add_f32_e32 v232, v232, v64
	v_add_f32_e32 v232, v232, v20
	v_add_f32_e32 v232, v232, v22
	v_add_f32_e32 v232, v232, v24
	v_fma_f32 v232, v232, s4, -v53
	v_cvt_pk_bf16_f32 v124, v124, v232
	ds_write_b16 v0, v124 offset:27040
	ds_write_b16_d16_hi v0, v124 offset:28080
	v_add_f32_e32 v124, 0, v52
	v_add_f32_e32 v124, v124, v53
	v_add_f32_e32 v124, v124, v55
	v_add_f32_e32 v124, v124, v57
	v_add_f32_e32 v124, v124, v54
	v_add_f32_e32 v124, v124, v56
	v_add_f32_e32 v124, v124, v58
	v_add_f32_e32 v124, v124, v59
	v_add_f32_e32 v124, v124, v60
	v_add_f32_e32 v124, v124, v61
	v_add_f32_e32 v124, v124, v63
	v_add_f32_e32 v124, v124, v65
	v_add_f32_e32 v124, v124, v62
	v_add_f32_e32 v124, v124, v64
	v_add_f32_e32 v124, v124, v20
	v_add_f32_e32 v124, v124, v22
	v_fma_f32 v124, v124, s4, -v52
	v_add_f32_e32 v232, 0, v51
	v_add_f32_e32 v232, v232, v52
	v_add_f32_e32 v232, v232, v53
	v_add_f32_e32 v232, v232, v55
	v_add_f32_e32 v232, v232, v57
	v_add_f32_e32 v232, v232, v54
	v_add_f32_e32 v232, v232, v56
	v_add_f32_e32 v232, v232, v58
	v_add_f32_e32 v232, v232, v59
	v_add_f32_e32 v232, v232, v60
	v_add_f32_e32 v232, v232, v61
	v_add_f32_e32 v232, v232, v63
	v_add_f32_e32 v232, v232, v65
	v_add_f32_e32 v232, v232, v62
	v_add_f32_e32 v232, v232, v64
	v_add_f32_e32 v232, v232, v20
	v_fma_f32 v232, v232, s4, -v51
	v_cvt_pk_bf16_f32 v124, v124, v232
	ds_write_b16 v0, v124 offset:29120
	ds_write_b16_d16_hi v0, v124 offset:30160
	v_add_f32_e32 v124, 0, v50
	v_add_f32_e32 v124, v124, v51
	v_add_f32_e32 v124, v124, v52
	v_add_f32_e32 v124, v124, v53
	v_add_f32_e32 v124, v124, v55
	v_add_f32_e32 v124, v124, v57
	v_add_f32_e32 v124, v124, v54
	v_add_f32_e32 v124, v124, v56
	v_add_f32_e32 v124, v124, v58
	v_add_f32_e32 v124, v124, v59
	v_add_f32_e32 v124, v124, v60
	v_add_f32_e32 v124, v124, v61
	v_add_f32_e32 v124, v124, v63
	v_add_f32_e32 v124, v124, v65
	v_add_f32_e32 v124, v124, v62
	v_add_f32_e32 v124, v124, v64
	v_fma_f32 v124, v124, s4, -v50
	v_add_f32_e32 v232, 0, v47
	v_add_f32_e32 v232, v232, v50
	v_add_f32_e32 v232, v232, v51
	v_add_f32_e32 v232, v232, v52
	v_add_f32_e32 v232, v232, v53
	v_add_f32_e32 v232, v232, v55
	v_add_f32_e32 v232, v232, v57
	v_add_f32_e32 v232, v232, v54
	v_add_f32_e32 v232, v232, v56
	v_add_f32_e32 v232, v232, v58
	v_add_f32_e32 v232, v232, v59
	v_add_f32_e32 v232, v232, v60
	v_add_f32_e32 v232, v232, v61
	v_add_f32_e32 v232, v232, v63
	v_add_f32_e32 v232, v232, v65
	v_add_f32_e32 v232, v232, v62
	v_fma_f32 v232, v232, s4, -v47
	v_cvt_pk_bf16_f32 v124, v124, v232
	ds_write_b16 v0, v124 offset:31200
	ds_write_b16_d16_hi v0, v124 offset:32240
	v_add_f32_e32 v124, 0, v44
	v_add_f32_e32 v124, v124, v47
	v_add_f32_e32 v124, v124, v50
	v_add_f32_e32 v124, v124, v51
	v_add_f32_e32 v124, v124, v52
	v_add_f32_e32 v124, v124, v53
	v_add_f32_e32 v124, v124, v55
	v_add_f32_e32 v124, v124, v57
	v_add_f32_e32 v124, v124, v54
	v_add_f32_e32 v124, v124, v56
	v_add_f32_e32 v124, v124, v58
	v_add_f32_e32 v124, v124, v59
	v_add_f32_e32 v124, v124, v60
	v_add_f32_e32 v124, v124, v61
	v_add_f32_e32 v124, v124, v63
	v_add_f32_e32 v124, v124, v65
	v_fma_f32 v124, v124, s4, -v44
	v_add_f32_e32 v232, 0, v48
	v_add_f32_e32 v232, v232, v44
	v_add_f32_e32 v232, v232, v47
	v_add_f32_e32 v232, v232, v50
	v_add_f32_e32 v232, v232, v51
	v_add_f32_e32 v232, v232, v52
	v_add_f32_e32 v232, v232, v53
	v_add_f32_e32 v232, v232, v55
	v_add_f32_e32 v232, v232, v57
	v_add_f32_e32 v232, v232, v54
	v_add_f32_e32 v232, v232, v56
	v_add_f32_e32 v232, v232, v58
	v_add_f32_e32 v232, v232, v59
	v_add_f32_e32 v232, v232, v60
	v_add_f32_e32 v232, v232, v61
	v_add_f32_e32 v232, v232, v63
	v_fma_f32 v232, v232, s4, -v48
	v_cvt_pk_bf16_f32 v124, v124, v232
	ds_write_b16 v0, v124 offset:33280
	ds_write_b16_d16_hi v0, v124 offset:34320
	v_add_f32_e32 v124, 0, v45
	v_add_f32_e32 v124, v124, v48
	v_add_f32_e32 v124, v124, v44
	v_add_f32_e32 v124, v124, v47
	v_add_f32_e32 v124, v124, v50
	v_add_f32_e32 v124, v124, v51
	v_add_f32_e32 v124, v124, v52
	v_add_f32_e32 v124, v124, v53
	v_add_f32_e32 v124, v124, v55
	v_add_f32_e32 v124, v124, v57
	v_add_f32_e32 v124, v124, v54
	v_add_f32_e32 v124, v124, v56
	v_add_f32_e32 v124, v124, v58
	v_add_f32_e32 v124, v124, v59
	v_add_f32_e32 v124, v124, v60
	v_add_f32_e32 v124, v124, v61
	v_fma_f32 v124, v124, s4, -v45
	v_add_f32_e32 v232, 0, v42
	v_add_f32_e32 v232, v232, v45
	v_add_f32_e32 v232, v232, v48
	v_add_f32_e32 v232, v232, v44
	v_add_f32_e32 v232, v232, v47
	v_add_f32_e32 v232, v232, v50
	v_add_f32_e32 v232, v232, v51
	v_add_f32_e32 v232, v232, v52
	v_add_f32_e32 v232, v232, v53
	v_add_f32_e32 v232, v232, v55
	v_add_f32_e32 v232, v232, v57
	v_add_f32_e32 v232, v232, v54
	v_add_f32_e32 v232, v232, v56
	v_add_f32_e32 v232, v232, v58
	v_add_f32_e32 v232, v232, v59
	v_add_f32_e32 v232, v232, v60
	v_fma_f32 v232, v232, s4, -v42
	v_cvt_pk_bf16_f32 v124, v124, v232
	ds_write_b16 v0, v124 offset:35360
	ds_write_b16_d16_hi v0, v124 offset:36400
	v_add_f32_e32 v124, 0, v40
	v_add_f32_e32 v124, v124, v42
	v_add_f32_e32 v124, v124, v45
	v_add_f32_e32 v124, v124, v48
	v_add_f32_e32 v124, v124, v44
	v_add_f32_e32 v124, v124, v47
	v_add_f32_e32 v124, v124, v50
	v_add_f32_e32 v124, v124, v51
	v_add_f32_e32 v124, v124, v52
	v_add_f32_e32 v124, v124, v53
	v_add_f32_e32 v124, v124, v55
	v_add_f32_e32 v124, v124, v57
	v_add_f32_e32 v124, v124, v54
	v_add_f32_e32 v124, v124, v56
	v_add_f32_e32 v124, v124, v58
	v_add_f32_e32 v124, v124, v59
	v_fma_f32 v124, v124, s4, -v40
	v_add_f32_e32 v232, 0, v37
	v_add_f32_e32 v232, v232, v40
	v_add_f32_e32 v232, v232, v42
	v_add_f32_e32 v232, v232, v45
	v_add_f32_e32 v232, v232, v48
	v_add_f32_e32 v232, v232, v44
	v_add_f32_e32 v232, v232, v47
	v_add_f32_e32 v232, v232, v50
	v_add_f32_e32 v232, v232, v51
	v_add_f32_e32 v232, v232, v52
	v_add_f32_e32 v232, v232, v53
	v_add_f32_e32 v232, v232, v55
	v_add_f32_e32 v232, v232, v57
	v_add_f32_e32 v232, v232, v54
	v_add_f32_e32 v232, v232, v56
	v_add_f32_e32 v232, v232, v58
	v_fma_f32 v232, v232, s4, -v37
	v_cvt_pk_bf16_f32 v124, v124, v232
	ds_write_b16 v0, v124 offset:37440
	ds_write_b16_d16_hi v0, v124 offset:38480
	v_add_f32_e32 v124, 0, v34
	v_add_f32_e32 v124, v124, v37
	v_add_f32_e32 v124, v124, v40
	v_add_f32_e32 v124, v124, v42
	v_add_f32_e32 v124, v124, v45
	v_add_f32_e32 v124, v124, v48
	v_add_f32_e32 v124, v124, v44
	v_add_f32_e32 v124, v124, v47
	v_add_f32_e32 v124, v124, v50
	v_add_f32_e32 v124, v124, v51
	v_add_f32_e32 v124, v124, v52
	v_add_f32_e32 v124, v124, v53
	v_add_f32_e32 v124, v124, v55
	v_add_f32_e32 v124, v124, v57
	v_add_f32_e32 v124, v124, v54
	v_add_f32_e32 v124, v124, v56
	v_fma_f32 v124, v124, s4, -v34
	v_add_f32_e32 v232, 0, v30
	v_add_f32_e32 v232, v232, v34
	v_add_f32_e32 v232, v232, v37
	v_add_f32_e32 v232, v232, v40
	v_add_f32_e32 v232, v232, v42
	v_add_f32_e32 v232, v232, v45
	v_add_f32_e32 v232, v232, v48
	v_add_f32_e32 v232, v232, v44
	v_add_f32_e32 v232, v232, v47
	v_add_f32_e32 v232, v232, v50
	v_add_f32_e32 v232, v232, v51
	v_add_f32_e32 v232, v232, v52
	v_add_f32_e32 v232, v232, v53
	v_add_f32_e32 v232, v232, v55
	v_add_f32_e32 v232, v232, v57
	v_add_f32_e32 v232, v232, v54
	v_fma_f32 v232, v232, s4, -v30
	v_cvt_pk_bf16_f32 v124, v124, v232
	ds_write_b16 v0, v124 offset:39520
	ds_write_b16_d16_hi v0, v124 offset:40560
	v_add_f32_e32 v124, 0, v27
	v_add_f32_e32 v124, v124, v30
	v_add_f32_e32 v124, v124, v34
	v_add_f32_e32 v124, v124, v37
	v_add_f32_e32 v124, v124, v40
	v_add_f32_e32 v124, v124, v42
	v_add_f32_e32 v124, v124, v45
	v_add_f32_e32 v124, v124, v48
	v_add_f32_e32 v124, v124, v44
	v_add_f32_e32 v124, v124, v47
	v_add_f32_e32 v124, v124, v50
	v_add_f32_e32 v124, v124, v51
	v_add_f32_e32 v124, v124, v52
	v_add_f32_e32 v124, v124, v53
	v_add_f32_e32 v124, v124, v55
	v_add_f32_e32 v124, v124, v57
	v_fma_f32 v124, v124, s4, -v27
	v_add_f32_e32 v232, 0, v31
	v_add_f32_e32 v232, v232, v27
	v_add_f32_e32 v232, v232, v30
	v_add_f32_e32 v232, v232, v34
	v_add_f32_e32 v232, v232, v37
	v_add_f32_e32 v232, v232, v40
	v_add_f32_e32 v232, v232, v42
	v_add_f32_e32 v232, v232, v45
	v_add_f32_e32 v232, v232, v48
	v_add_f32_e32 v232, v232, v44
	v_add_f32_e32 v232, v232, v47
	v_add_f32_e32 v232, v232, v50
	v_add_f32_e32 v232, v232, v51
	v_add_f32_e32 v232, v232, v52
	v_add_f32_e32 v232, v232, v53
	v_add_f32_e32 v232, v232, v55
	v_fma_f32 v232, v232, s4, -v31
	v_cvt_pk_bf16_f32 v124, v124, v232
	ds_write_b16 v0, v124 offset:41600
	ds_write_b16_d16_hi v0, v124 offset:42640
	v_add_f32_e32 v124, 0, v28
	v_add_f32_e32 v124, v124, v31
	v_add_f32_e32 v124, v124, v27
	v_add_f32_e32 v124, v124, v30
	v_add_f32_e32 v124, v124, v34
	v_add_f32_e32 v124, v124, v37
	v_add_f32_e32 v124, v124, v40
	v_add_f32_e32 v124, v124, v42
	v_add_f32_e32 v124, v124, v45
	v_add_f32_e32 v124, v124, v48
	v_add_f32_e32 v124, v124, v44
	v_add_f32_e32 v124, v124, v47
	v_add_f32_e32 v124, v124, v50
	v_add_f32_e32 v124, v124, v51
	v_add_f32_e32 v124, v124, v52
	v_add_f32_e32 v124, v124, v53
	v_fma_f32 v124, v124, s4, -v28
	v_add_f32_e32 v232, 0, v25
	v_add_f32_e32 v232, v232, v28
	v_add_f32_e32 v232, v232, v31
	v_add_f32_e32 v232, v232, v27
	v_add_f32_e32 v232, v232, v30
	v_add_f32_e32 v232, v232, v34
	v_add_f32_e32 v232, v232, v37
	v_add_f32_e32 v232, v232, v40
	v_add_f32_e32 v232, v232, v42
	v_add_f32_e32 v232, v232, v45
	v_add_f32_e32 v232, v232, v48
	v_add_f32_e32 v232, v232, v44
	v_add_f32_e32 v232, v232, v47
	v_add_f32_e32 v232, v232, v50
	v_add_f32_e32 v232, v232, v51
	v_add_f32_e32 v232, v232, v52
	v_fma_f32 v232, v232, s4, -v25
	v_cvt_pk_bf16_f32 v124, v124, v232
	ds_write_b16 v0, v124 offset:43680
	ds_write_b16_d16_hi v0, v124 offset:44720
	v_add_f32_e32 v124, 0, v23
	v_add_f32_e32 v124, v124, v25
	v_add_f32_e32 v124, v124, v28
	v_add_f32_e32 v124, v124, v31
	v_add_f32_e32 v124, v124, v27
	v_add_f32_e32 v124, v124, v30
	v_add_f32_e32 v124, v124, v34
	v_add_f32_e32 v124, v124, v37
	v_add_f32_e32 v124, v124, v40
	v_add_f32_e32 v124, v124, v42
	v_add_f32_e32 v124, v124, v45
	v_add_f32_e32 v124, v124, v48
	v_add_f32_e32 v124, v124, v44
	v_add_f32_e32 v124, v124, v47
	v_add_f32_e32 v124, v124, v50
	v_add_f32_e32 v124, v124, v51
	v_fma_f32 v124, v124, s4, -v23
	v_add_f32_e32 v232, 0, v21
	v_add_f32_e32 v232, v232, v23
	v_add_f32_e32 v232, v232, v25
	v_add_f32_e32 v232, v232, v28
	v_add_f32_e32 v232, v232, v31
	v_add_f32_e32 v232, v232, v27
	v_add_f32_e32 v232, v232, v30
	v_add_f32_e32 v232, v232, v34
	v_add_f32_e32 v232, v232, v37
	v_add_f32_e32 v232, v232, v40
	v_add_f32_e32 v232, v232, v42
	v_add_f32_e32 v232, v232, v45
	v_add_f32_e32 v232, v232, v48
	v_add_f32_e32 v232, v232, v44
	v_add_f32_e32 v232, v232, v47
	v_add_f32_e32 v232, v232, v50
	v_fma_f32 v232, v232, s4, -v21
	v_cvt_pk_bf16_f32 v124, v124, v232
	ds_write_b16 v0, v124 offset:45760
	ds_write_b16_d16_hi v0, v124 offset:46800
	v_add_f32_e32 v124, 0, v19
	v_add_f32_e32 v124, v124, v21
	v_add_f32_e32 v124, v124, v23
	v_add_f32_e32 v124, v124, v25
	v_add_f32_e32 v124, v124, v28
	v_add_f32_e32 v124, v124, v31
	v_add_f32_e32 v124, v124, v27
	v_add_f32_e32 v124, v124, v30
	v_add_f32_e32 v124, v124, v34
	v_add_f32_e32 v124, v124, v37
	v_add_f32_e32 v124, v124, v40
	v_add_f32_e32 v124, v124, v42
	v_add_f32_e32 v124, v124, v45
	v_add_f32_e32 v124, v124, v48
	v_add_f32_e32 v124, v124, v44
	v_add_f32_e32 v124, v124, v47
	v_fma_f32 v124, v124, s4, -v19
	v_add_f32_e32 v232, 0, v18
	v_add_f32_e32 v232, v232, v19
	v_add_f32_e32 v232, v232, v21
	v_add_f32_e32 v232, v232, v23
	v_add_f32_e32 v232, v232, v25
	v_add_f32_e32 v232, v232, v28
	v_add_f32_e32 v232, v232, v31
	v_add_f32_e32 v232, v232, v27
	v_add_f32_e32 v232, v232, v30
	v_add_f32_e32 v232, v232, v34
	v_add_f32_e32 v232, v232, v37
	v_add_f32_e32 v232, v232, v40
	v_add_f32_e32 v232, v232, v42
	v_add_f32_e32 v232, v232, v45
	v_add_f32_e32 v232, v232, v48
	v_add_f32_e32 v232, v232, v44
	v_fma_f32 v232, v232, s4, -v18
	v_cvt_pk_bf16_f32 v124, v124, v232
	ds_write_b16 v0, v124 offset:47840
	ds_write_b16_d16_hi v0, v124 offset:48880
	v_add_f32_e32 v124, 0, v16
	v_add_f32_e32 v124, v124, v18
	v_add_f32_e32 v124, v124, v19
	v_add_f32_e32 v124, v124, v21
	v_add_f32_e32 v124, v124, v23
	v_add_f32_e32 v124, v124, v25
	v_add_f32_e32 v124, v124, v28
	v_add_f32_e32 v124, v124, v31
	v_add_f32_e32 v124, v124, v27
	v_add_f32_e32 v124, v124, v30
	v_add_f32_e32 v124, v124, v34
	v_add_f32_e32 v124, v124, v37
	v_add_f32_e32 v124, v124, v40
	v_add_f32_e32 v124, v124, v42
	v_add_f32_e32 v124, v124, v45
	v_add_f32_e32 v124, v124, v48
	v_fma_f32 v124, v124, s4, -v16
	v_add_f32_e32 v232, 0, v14
	v_add_f32_e32 v232, v232, v16
	v_add_f32_e32 v232, v232, v18
	v_add_f32_e32 v232, v232, v19
	v_add_f32_e32 v232, v232, v21
	v_add_f32_e32 v232, v232, v23
	v_add_f32_e32 v232, v232, v25
	v_add_f32_e32 v232, v232, v28
	v_add_f32_e32 v232, v232, v31
	v_add_f32_e32 v232, v232, v27
	v_add_f32_e32 v232, v232, v30
	v_add_f32_e32 v232, v232, v34
	v_add_f32_e32 v232, v232, v37
	v_add_f32_e32 v232, v232, v40
	v_add_f32_e32 v232, v232, v42
	v_add_f32_e32 v232, v232, v45
	v_fma_f32 v232, v232, s4, -v14
	v_cvt_pk_bf16_f32 v124, v124, v232
	ds_write_b16 v0, v124 offset:49920
	ds_write_b16_d16_hi v0, v124 offset:50960
	v_add_f32_e32 v124, 0, v12
	v_add_f32_e32 v124, v124, v14
	v_add_f32_e32 v124, v124, v16
	v_add_f32_e32 v124, v124, v18
	v_add_f32_e32 v124, v124, v19
	v_add_f32_e32 v124, v124, v21
	v_add_f32_e32 v124, v124, v23
	v_add_f32_e32 v124, v124, v25
	v_add_f32_e32 v124, v124, v28
	v_add_f32_e32 v124, v124, v31
	v_add_f32_e32 v124, v124, v27
	v_add_f32_e32 v124, v124, v30
	v_add_f32_e32 v124, v124, v34
	v_add_f32_e32 v124, v124, v37
	v_add_f32_e32 v124, v124, v40
	v_add_f32_e32 v124, v124, v42
	v_fma_f32 v124, v124, s4, -v12
	v_add_f32_e32 v232, 0, v9
	v_add_f32_e32 v232, v232, v12
	v_add_f32_e32 v232, v232, v14
	v_add_f32_e32 v232, v232, v16
	v_add_f32_e32 v232, v232, v18
	v_add_f32_e32 v232, v232, v19
	v_add_f32_e32 v232, v232, v21
	v_add_f32_e32 v232, v232, v23
	v_add_f32_e32 v232, v232, v25
	v_add_f32_e32 v232, v232, v28
	v_add_f32_e32 v232, v232, v31
	v_add_f32_e32 v232, v232, v27
	v_add_f32_e32 v232, v232, v30
	v_add_f32_e32 v232, v232, v34
	v_add_f32_e32 v232, v232, v37
	v_add_f32_e32 v232, v232, v40
	v_fma_f32 v232, v232, s4, -v9
	v_cvt_pk_bf16_f32 v124, v124, v232
	ds_write_b16 v0, v124 offset:52000
	ds_write_b16_d16_hi v0, v124 offset:53040
	v_add_f32_e32 v124, 0, v7
	v_add_f32_e32 v124, v124, v9
	v_add_f32_e32 v124, v124, v12
	v_add_f32_e32 v124, v124, v14
	v_add_f32_e32 v124, v124, v16
	v_add_f32_e32 v124, v124, v18
	v_add_f32_e32 v124, v124, v19
	v_add_f32_e32 v124, v124, v21
	v_add_f32_e32 v124, v124, v23
	v_add_f32_e32 v124, v124, v25
	v_add_f32_e32 v124, v124, v28
	v_add_f32_e32 v124, v124, v31
	v_add_f32_e32 v124, v124, v27
	v_add_f32_e32 v124, v124, v30
	v_add_f32_e32 v124, v124, v34
	v_add_f32_e32 v124, v124, v37
	v_fma_f32 v124, v124, s4, -v7
	v_add_f32_e32 v232, 0, v5
	v_add_f32_e32 v232, v232, v7
	v_add_f32_e32 v232, v232, v9
	v_add_f32_e32 v232, v232, v12
	v_add_f32_e32 v232, v232, v14
	v_add_f32_e32 v232, v232, v16
	v_add_f32_e32 v232, v232, v18
	v_add_f32_e32 v232, v232, v19
	v_add_f32_e32 v232, v232, v21
	v_add_f32_e32 v232, v232, v23
	v_add_f32_e32 v232, v232, v25
	v_add_f32_e32 v232, v232, v28
	v_add_f32_e32 v232, v232, v31
	v_add_f32_e32 v232, v232, v27
	v_add_f32_e32 v232, v232, v30
	v_add_f32_e32 v232, v232, v34
	v_fma_f32 v232, v232, s4, -v5
	v_cvt_pk_bf16_f32 v124, v124, v232
	ds_write_b16 v0, v124 offset:54080
	ds_write_b16_d16_hi v0, v124 offset:55120
	v_add_f32_e32 v124, 0, v3
	v_add_f32_e32 v124, v124, v5
	v_add_f32_e32 v124, v124, v7
	v_add_f32_e32 v124, v124, v9
	v_add_f32_e32 v124, v124, v12
	v_add_f32_e32 v124, v124, v14
	v_add_f32_e32 v124, v124, v16
	v_add_f32_e32 v124, v124, v18
	v_add_f32_e32 v124, v124, v19
	v_add_f32_e32 v124, v124, v21
	v_add_f32_e32 v124, v124, v23
	v_add_f32_e32 v124, v124, v25
	v_add_f32_e32 v124, v124, v28
	v_add_f32_e32 v124, v124, v31
	v_add_f32_e32 v124, v124, v27
	v_add_f32_e32 v124, v124, v30
	v_fma_f32 v124, v124, s4, -v3
	v_add_f32_e32 v232, 0, v17
	v_add_f32_e32 v232, v232, v3
	v_add_f32_e32 v232, v232, v5
	v_add_f32_e32 v232, v232, v7
	v_add_f32_e32 v232, v232, v9
	v_add_f32_e32 v232, v232, v12
	v_add_f32_e32 v232, v232, v14
	v_add_f32_e32 v232, v232, v16
	v_add_f32_e32 v232, v232, v18
	v_add_f32_e32 v232, v232, v19
	v_add_f32_e32 v232, v232, v21
	v_add_f32_e32 v232, v232, v23
	v_add_f32_e32 v232, v232, v25
	v_add_f32_e32 v232, v232, v28
	v_add_f32_e32 v232, v232, v31
	v_add_f32_e32 v232, v232, v27
	v_fma_f32 v232, v232, s4, -v17
	v_cvt_pk_bf16_f32 v124, v124, v232
	ds_write_b16 v0, v124 offset:56160
	ds_write_b16_d16_hi v0, v124 offset:57200
	v_add_f32_e32 v124, 0, v15
	v_add_f32_e32 v124, v124, v17
	v_add_f32_e32 v124, v124, v3
	v_add_f32_e32 v124, v124, v5
	v_add_f32_e32 v124, v124, v7
	v_add_f32_e32 v124, v124, v9
	v_add_f32_e32 v124, v124, v12
	v_add_f32_e32 v124, v124, v14
	v_add_f32_e32 v124, v124, v16
	v_add_f32_e32 v124, v124, v18
	v_add_f32_e32 v124, v124, v19
	v_add_f32_e32 v124, v124, v21
	v_add_f32_e32 v124, v124, v23
	v_add_f32_e32 v124, v124, v25
	v_add_f32_e32 v124, v124, v28
	v_add_f32_e32 v124, v124, v31
	v_fma_f32 v124, v124, s4, -v15
	v_add_f32_e32 v232, 0, v13
	v_add_f32_e32 v232, v232, v15
	v_add_f32_e32 v232, v232, v17
	v_add_f32_e32 v232, v232, v3
	v_add_f32_e32 v232, v232, v5
	v_add_f32_e32 v232, v232, v7
	v_add_f32_e32 v232, v232, v9
	v_add_f32_e32 v232, v232, v12
	v_add_f32_e32 v232, v232, v14
	v_add_f32_e32 v232, v232, v16
	v_add_f32_e32 v232, v232, v18
	v_add_f32_e32 v232, v232, v19
	v_add_f32_e32 v232, v232, v21
	v_add_f32_e32 v232, v232, v23
	v_add_f32_e32 v232, v232, v25
	v_add_f32_e32 v232, v232, v28
	v_fma_f32 v232, v232, s4, -v13
	v_cvt_pk_bf16_f32 v124, v124, v232
	ds_write_b16 v0, v124 offset:58240
	ds_write_b16_d16_hi v0, v124 offset:59280
	v_add_f32_e32 v124, 0, v11
	v_add_f32_e32 v124, v124, v13
	v_add_f32_e32 v124, v124, v15
	v_add_f32_e32 v124, v124, v17
	v_add_f32_e32 v124, v124, v3
	v_add_f32_e32 v124, v124, v5
	v_add_f32_e32 v124, v124, v7
	v_add_f32_e32 v124, v124, v9
	v_add_f32_e32 v124, v124, v12
	v_add_f32_e32 v124, v124, v14
	v_add_f32_e32 v124, v124, v16
	v_add_f32_e32 v124, v124, v18
	v_add_f32_e32 v124, v124, v19
	v_add_f32_e32 v124, v124, v21
	v_add_f32_e32 v124, v124, v23
	v_add_f32_e32 v124, v124, v25
	v_fma_f32 v124, v124, s4, -v11
	v_add_f32_e32 v232, 0, v10
	v_add_f32_e32 v232, v232, v11
	v_add_f32_e32 v232, v232, v13
	v_add_f32_e32 v232, v232, v15
	v_add_f32_e32 v232, v232, v17
	v_add_f32_e32 v232, v232, v3
	v_add_f32_e32 v232, v232, v5
	v_add_f32_e32 v232, v232, v7
	v_add_f32_e32 v232, v232, v9
	v_add_f32_e32 v232, v232, v12
	v_add_f32_e32 v232, v232, v14
	v_add_f32_e32 v232, v232, v16
	v_add_f32_e32 v232, v232, v18
	v_add_f32_e32 v232, v232, v19
	v_add_f32_e32 v232, v232, v21
	v_add_f32_e32 v232, v232, v23
	v_fma_f32 v232, v232, s4, -v10
	v_cvt_pk_bf16_f32 v124, v124, v232
	ds_write_b16 v0, v124 offset:60320
	ds_write_b16_d16_hi v0, v124 offset:61360
	v_add_f32_e32 v124, 0, v8
	v_add_f32_e32 v124, v124, v10
	v_add_f32_e32 v124, v124, v11
	v_add_f32_e32 v124, v124, v13
	v_add_f32_e32 v124, v124, v15
	v_add_f32_e32 v124, v124, v17
	v_add_f32_e32 v124, v124, v3
	v_add_f32_e32 v124, v124, v5
	v_add_f32_e32 v124, v124, v7
	v_add_f32_e32 v124, v124, v9
	v_add_f32_e32 v124, v124, v12
	v_add_f32_e32 v124, v124, v14
	v_add_f32_e32 v124, v124, v16
	v_add_f32_e32 v124, v124, v18
	v_add_f32_e32 v124, v124, v19
	v_add_f32_e32 v124, v124, v21
	v_fma_f32 v124, v124, s4, -v8
	v_add_f32_e32 v232, 0, v6
	v_add_f32_e32 v232, v232, v8
	v_add_f32_e32 v232, v232, v10
	v_add_f32_e32 v232, v232, v11
	v_add_f32_e32 v232, v232, v13
	v_add_f32_e32 v232, v232, v15
	v_add_f32_e32 v232, v232, v17
	v_add_f32_e32 v232, v232, v3
	v_add_f32_e32 v232, v232, v5
	v_add_f32_e32 v232, v232, v7
	v_add_f32_e32 v232, v232, v9
	v_add_f32_e32 v232, v232, v12
	v_add_f32_e32 v232, v232, v14
	v_add_f32_e32 v232, v232, v16
	v_add_f32_e32 v232, v232, v18
	v_add_f32_e32 v232, v232, v19
	v_fma_f32 v232, v232, s4, -v6
	v_cvt_pk_bf16_f32 v124, v124, v232
	ds_write_b16 v0, v124 offset:62400
	ds_write_b16_d16_hi v0, v124 offset:63440
	v_add_f32_e32 v124, 0, v4
	v_add_f32_e32 v124, v124, v6
	v_add_f32_e32 v124, v124, v8
	v_add_f32_e32 v124, v124, v10
	v_add_f32_e32 v124, v124, v11
	v_add_f32_e32 v124, v124, v13
	v_add_f32_e32 v124, v124, v15
	v_add_f32_e32 v124, v124, v17
	v_add_f32_e32 v124, v124, v3
	v_add_f32_e32 v124, v124, v5
	v_add_f32_e32 v124, v124, v7
	v_add_f32_e32 v124, v124, v9
	v_add_f32_e32 v124, v124, v12
	v_add_f32_e32 v124, v124, v14
	v_add_f32_e32 v124, v124, v16
	v_add_f32_e32 v124, v124, v18
	v_fma_f32 v124, v124, s4, -v4
	v_cvt_pk_bf16_f32 v124, v124, s0
	ds_write_b16 v0, v124 offset:64480
	v_add_f32_e32 v124, 0, v2
	v_add_f32_e32 v124, v124, v4
	v_add_f32_e32 v124, v124, v6
	v_add_f32_e32 v124, v124, v8
	v_add_f32_e32 v124, v124, v10
	v_add_f32_e32 v124, v124, v11
	v_add_f32_e32 v124, v124, v13
	v_add_f32_e32 v124, v124, v15
	v_add_f32_e32 v124, v124, v17
	v_add_f32_e32 v124, v124, v3
	v_add_f32_e32 v124, v124, v5
	v_add_f32_e32 v124, v124, v7
	v_add_f32_e32 v124, v124, v9
	v_add_f32_e32 v124, v124, v12
	v_add_f32_e32 v124, v124, v14
	v_add_f32_e32 v124, v124, v16
	v_mul_f32_e32 v137, 0x3d800000, v124
	s_cbranch_execz .LBB0_593
	s_branch .LBB0_594

.LBB0_593:
	v_mov_b32_e32 v125, 0x3e800000
	v_cndmask_b32_e64 v124, v125, 1.0, s[6:7]
	v_fma_f32 v123, v124, v123, -v49
	v_cvt_pk_bf16_f32 v123, v123, s0
	ds_write_b16 v0, v123
	v_add_f32_e32 v123, 0, v46
	v_add_f32_e32 v123, v123, v49
	v_add_f32_e32 v123, v123, v115
	v_add_f32_e32 v122, v123, v122
	v_cndmask_b32_e64 v123, v125, 0.5, s[6:7]
	v_fma_f32 v122, v123, v122, -v46
	v_cvt_pk_bf16_f32 v122, v122, s0
	ds_write_b16 v0, v122 offset:1040
	v_add_f32_e32 v122, 0, v43
	v_add_f32_e32 v122, v122, v46
	v_add_f32_e32 v122, v122, v49
	v_add_f32_e32 v115, v122, v115
	v_mov_b32_e32 v122, 0x3eaaaaab
	v_cndmask_b32_e64 v122, v125, v122, s[6:7]
	v_fma_f32 v115, v122, v115, -v43
	v_add_f32_e32 v232, 0, v41
	v_add_f32_e32 v232, v232, v43
	v_add_f32_e32 v232, v232, v46
	v_add_f32_e32 v232, v232, v49
	v_fma_f32 v232, v232, s97, -v41
	v_cvt_pk_bf16_f32 v115, v115, v232
	ds_write_b16 v0, v115 offset:2080
	ds_write_b16_d16_hi v0, v115 offset:3120
	v_add_f32_e32 v115, 0, v38
	v_add_f32_e32 v115, v115, v41
	v_add_f32_e32 v115, v115, v43
	v_add_f32_e32 v115, v115, v46
	v_fma_f32 v115, v115, s97, -v38
	v_add_f32_e32 v232, 0, v35
	v_add_f32_e32 v232, v232, v38
	v_add_f32_e32 v232, v232, v41
	v_add_f32_e32 v232, v232, v43
	v_fma_f32 v232, v232, s97, -v35
	v_cvt_pk_bf16_f32 v115, v115, v232
	ds_write_b16 v0, v115 offset:4160
	ds_write_b16_d16_hi v0, v115 offset:5200
	v_add_f32_e32 v115, 0, v32
	v_add_f32_e32 v115, v115, v35
	v_add_f32_e32 v115, v115, v38
	v_add_f32_e32 v115, v115, v41
	v_fma_f32 v115, v115, s97, -v32
	v_add_f32_e32 v232, 0, v39
	v_add_f32_e32 v232, v232, v32
	v_add_f32_e32 v232, v232, v35
	v_add_f32_e32 v232, v232, v38
	v_fma_f32 v232, v232, s97, -v39
	v_cvt_pk_bf16_f32 v115, v115, v232
	ds_write_b16 v0, v115 offset:6240
	ds_write_b16_d16_hi v0, v115 offset:7280
	v_add_f32_e32 v115, 0, v36
	v_add_f32_e32 v115, v115, v39
	v_add_f32_e32 v115, v115, v32
	v_add_f32_e32 v115, v115, v35
	v_fma_f32 v115, v115, s97, -v36
	v_add_f32_e32 v232, 0, v33
	v_add_f32_e32 v232, v232, v36
	v_add_f32_e32 v232, v232, v39
	v_add_f32_e32 v232, v232, v32
	v_fma_f32 v232, v232, s97, -v33
	v_cvt_pk_bf16_f32 v115, v115, v232
	ds_write_b16 v0, v115 offset:8320
	ds_write_b16_d16_hi v0, v115 offset:9360
	v_add_f32_e32 v115, 0, v29
	v_add_f32_e32 v115, v115, v33
	v_add_f32_e32 v115, v115, v36
	v_add_f32_e32 v115, v115, v39
	v_fma_f32 v115, v115, s97, -v29
	v_add_f32_e32 v232, 0, v26
	v_add_f32_e32 v232, v232, v29
	v_add_f32_e32 v232, v232, v33
	v_add_f32_e32 v232, v232, v36
	v_fma_f32 v232, v232, s97, -v26
	v_cvt_pk_bf16_f32 v115, v115, v232
	ds_write_b16 v0, v115 offset:10400
	ds_write_b16_d16_hi v0, v115 offset:11440
	v_add_f32_e32 v115, 0, v24
	v_add_f32_e32 v115, v115, v26
	v_add_f32_e32 v115, v115, v29
	v_add_f32_e32 v115, v115, v33
	v_fma_f32 v115, v115, s97, -v24
	v_add_f32_e32 v232, 0, v22
	v_add_f32_e32 v232, v232, v24
	v_add_f32_e32 v232, v232, v26
	v_add_f32_e32 v232, v232, v29
	v_fma_f32 v232, v232, s97, -v22
	v_cvt_pk_bf16_f32 v115, v115, v232
	ds_write_b16 v0, v115 offset:12480
	ds_write_b16_d16_hi v0, v115 offset:13520
	v_add_f32_e32 v115, 0, v20
	v_add_f32_e32 v115, v115, v22
	v_add_f32_e32 v115, v115, v24
	v_add_f32_e32 v115, v115, v26
	v_fma_f32 v115, v115, s97, -v20
	v_add_f32_e32 v232, 0, v64
	v_add_f32_e32 v232, v232, v20
	v_add_f32_e32 v232, v232, v22
	v_add_f32_e32 v232, v232, v24
	v_fma_f32 v232, v232, s97, -v64
	v_cvt_pk_bf16_f32 v115, v115, v232
	ds_write_b16 v0, v115 offset:14560
	ds_write_b16_d16_hi v0, v115 offset:15600
	v_add_f32_e32 v115, 0, v62
	v_add_f32_e32 v115, v115, v64
	v_add_f32_e32 v115, v115, v20
	v_add_f32_e32 v115, v115, v22
	v_fma_f32 v115, v115, s97, -v62
	v_add_f32_e32 v232, 0, v65
	v_add_f32_e32 v232, v232, v62
	v_add_f32_e32 v232, v232, v64
	v_add_f32_e32 v232, v232, v20
	v_fma_f32 v232, v232, s97, -v65
	v_cvt_pk_bf16_f32 v115, v115, v232
	ds_write_b16 v0, v115 offset:16640
	ds_write_b16_d16_hi v0, v115 offset:17680
	v_add_f32_e32 v115, 0, v63
	v_add_f32_e32 v115, v115, v65
	v_add_f32_e32 v115, v115, v62
	v_add_f32_e32 v115, v115, v64
	v_fma_f32 v115, v115, s97, -v63
	v_add_f32_e32 v232, 0, v61
	v_add_f32_e32 v232, v232, v63
	v_add_f32_e32 v232, v232, v65
	v_add_f32_e32 v232, v232, v62
	v_fma_f32 v232, v232, s97, -v61
	v_cvt_pk_bf16_f32 v115, v115, v232
	ds_write_b16 v0, v115 offset:18720
	ds_write_b16_d16_hi v0, v115 offset:19760
	v_add_f32_e32 v115, 0, v60
	v_add_f32_e32 v115, v115, v61
	v_add_f32_e32 v115, v115, v63
	v_add_f32_e32 v115, v115, v65
	v_fma_f32 v115, v115, s97, -v60
	v_add_f32_e32 v232, 0, v59
	v_add_f32_e32 v232, v232, v60
	v_add_f32_e32 v232, v232, v61
	v_add_f32_e32 v232, v232, v63
	v_fma_f32 v232, v232, s97, -v59
	v_cvt_pk_bf16_f32 v115, v115, v232
	ds_write_b16 v0, v115 offset:20800
	ds_write_b16_d16_hi v0, v115 offset:21840
	v_add_f32_e32 v115, 0, v58
	v_add_f32_e32 v115, v115, v59
	v_add_f32_e32 v115, v115, v60
	v_add_f32_e32 v115, v115, v61
	v_fma_f32 v115, v115, s97, -v58
	v_add_f32_e32 v232, 0, v56
	v_add_f32_e32 v232, v232, v58
	v_add_f32_e32 v232, v232, v59
	v_add_f32_e32 v232, v232, v60
	v_fma_f32 v232, v232, s97, -v56
	v_cvt_pk_bf16_f32 v115, v115, v232
	ds_write_b16 v0, v115 offset:22880
	ds_write_b16_d16_hi v0, v115 offset:23920
	v_add_f32_e32 v115, 0, v54
	v_add_f32_e32 v115, v115, v56
	v_add_f32_e32 v115, v115, v58
	v_add_f32_e32 v115, v115, v59
	v_fma_f32 v115, v115, s97, -v54
	v_add_f32_e32 v232, 0, v57
	v_add_f32_e32 v232, v232, v54
	v_add_f32_e32 v232, v232, v56
	v_add_f32_e32 v232, v232, v58
	v_fma_f32 v232, v232, s97, -v57
	v_cvt_pk_bf16_f32 v115, v115, v232
	ds_write_b16 v0, v115 offset:24960
	ds_write_b16_d16_hi v0, v115 offset:26000
	v_add_f32_e32 v115, 0, v55
	v_add_f32_e32 v115, v115, v57
	v_add_f32_e32 v115, v115, v54
	v_add_f32_e32 v115, v115, v56
	v_fma_f32 v115, v115, s97, -v55
	v_add_f32_e32 v232, 0, v53
	v_add_f32_e32 v232, v232, v55
	v_add_f32_e32 v232, v232, v57
	v_add_f32_e32 v232, v232, v54
	v_fma_f32 v232, v232, s97, -v53
	v_cvt_pk_bf16_f32 v115, v115, v232
	ds_write_b16 v0, v115 offset:27040
	ds_write_b16_d16_hi v0, v115 offset:28080
	v_add_f32_e32 v115, 0, v52
	v_add_f32_e32 v115, v115, v53
	v_add_f32_e32 v115, v115, v55
	v_add_f32_e32 v115, v115, v57
	v_fma_f32 v115, v115, s97, -v52
	v_add_f32_e32 v232, 0, v51
	v_add_f32_e32 v232, v232, v52
	v_add_f32_e32 v232, v232, v53
	v_add_f32_e32 v232, v232, v55
	v_fma_f32 v232, v232, s97, -v51
	v_cvt_pk_bf16_f32 v115, v115, v232
	ds_write_b16 v0, v115 offset:29120
	ds_write_b16_d16_hi v0, v115 offset:30160
	v_add_f32_e32 v115, 0, v50
	v_add_f32_e32 v115, v115, v51
	v_add_f32_e32 v115, v115, v52
	v_add_f32_e32 v115, v115, v53
	v_fma_f32 v115, v115, s97, -v50
	v_add_f32_e32 v232, 0, v47
	v_add_f32_e32 v232, v232, v50
	v_add_f32_e32 v232, v232, v51
	v_add_f32_e32 v232, v232, v52
	v_fma_f32 v232, v232, s97, -v47
	v_cvt_pk_bf16_f32 v115, v115, v232
	ds_write_b16 v0, v115 offset:31200
	ds_write_b16_d16_hi v0, v115 offset:32240
	v_add_f32_e32 v115, 0, v44
	v_add_f32_e32 v115, v115, v47
	v_add_f32_e32 v115, v115, v50
	v_add_f32_e32 v115, v115, v51
	v_fma_f32 v115, v115, s97, -v44
	v_add_f32_e32 v232, 0, v48
	v_add_f32_e32 v232, v232, v44
	v_add_f32_e32 v232, v232, v47
	v_add_f32_e32 v232, v232, v50
	v_fma_f32 v232, v232, s97, -v48
	v_cvt_pk_bf16_f32 v115, v115, v232
	ds_write_b16 v0, v115 offset:33280
	ds_write_b16_d16_hi v0, v115 offset:34320
	v_add_f32_e32 v115, 0, v45
	v_add_f32_e32 v115, v115, v48
	v_add_f32_e32 v115, v115, v44
	v_add_f32_e32 v115, v115, v47
	v_fma_f32 v115, v115, s97, -v45
	v_add_f32_e32 v232, 0, v42
	v_add_f32_e32 v232, v232, v45
	v_add_f32_e32 v232, v232, v48
	v_add_f32_e32 v232, v232, v44
	v_fma_f32 v232, v232, s97, -v42
	v_cvt_pk_bf16_f32 v115, v115, v232
	ds_write_b16 v0, v115 offset:35360
	ds_write_b16_d16_hi v0, v115 offset:36400
	v_add_f32_e32 v115, 0, v40
	v_add_f32_e32 v115, v115, v42
	v_add_f32_e32 v115, v115, v45
	v_add_f32_e32 v115, v115, v48
	v_fma_f32 v115, v115, s97, -v40
	v_add_f32_e32 v232, 0, v37
	v_add_f32_e32 v232, v232, v40
	v_add_f32_e32 v232, v232, v42
	v_add_f32_e32 v232, v232, v45
	v_fma_f32 v232, v232, s97, -v37
	v_cvt_pk_bf16_f32 v115, v115, v232
	ds_write_b16 v0, v115 offset:37440
	ds_write_b16_d16_hi v0, v115 offset:38480
	v_add_f32_e32 v115, 0, v34
	v_add_f32_e32 v115, v115, v37
	v_add_f32_e32 v115, v115, v40
	v_add_f32_e32 v115, v115, v42
	v_fma_f32 v115, v115, s97, -v34
	v_add_f32_e32 v232, 0, v30
	v_add_f32_e32 v232, v232, v34
	v_add_f32_e32 v232, v232, v37
	v_add_f32_e32 v232, v232, v40
	v_fma_f32 v232, v232, s97, -v30
	v_cvt_pk_bf16_f32 v115, v115, v232
	ds_write_b16 v0, v115 offset:39520
	ds_write_b16_d16_hi v0, v115 offset:40560
	v_add_f32_e32 v115, 0, v27
	v_add_f32_e32 v115, v115, v30
	v_add_f32_e32 v115, v115, v34
	v_add_f32_e32 v115, v115, v37
	v_fma_f32 v115, v115, s97, -v27
	v_add_f32_e32 v232, 0, v31
	v_add_f32_e32 v232, v232, v27
	v_add_f32_e32 v232, v232, v30
	v_add_f32_e32 v232, v232, v34
	v_fma_f32 v232, v232, s97, -v31
	v_cvt_pk_bf16_f32 v115, v115, v232
	ds_write_b16 v0, v115 offset:41600
	ds_write_b16_d16_hi v0, v115 offset:42640
	v_add_f32_e32 v115, 0, v28
	v_add_f32_e32 v115, v115, v31
	v_add_f32_e32 v115, v115, v27
	v_add_f32_e32 v115, v115, v30
	v_fma_f32 v115, v115, s97, -v28
	v_add_f32_e32 v232, 0, v25
	v_add_f32_e32 v232, v232, v28
	v_add_f32_e32 v232, v232, v31
	v_add_f32_e32 v232, v232, v27
	v_fma_f32 v232, v232, s97, -v25
	v_cvt_pk_bf16_f32 v115, v115, v232
	ds_write_b16 v0, v115 offset:43680
	ds_write_b16_d16_hi v0, v115 offset:44720
	v_add_f32_e32 v115, 0, v23
	v_add_f32_e32 v115, v115, v25
	v_add_f32_e32 v115, v115, v28
	v_add_f32_e32 v115, v115, v31
	v_fma_f32 v115, v115, s97, -v23
	v_add_f32_e32 v232, 0, v21
	v_add_f32_e32 v232, v232, v23
	v_add_f32_e32 v232, v232, v25
	v_add_f32_e32 v232, v232, v28
	v_fma_f32 v232, v232, s97, -v21
	v_cvt_pk_bf16_f32 v115, v115, v232
	ds_write_b16 v0, v115 offset:45760
	ds_write_b16_d16_hi v0, v115 offset:46800
	v_add_f32_e32 v115, 0, v19
	v_add_f32_e32 v115, v115, v21
	v_add_f32_e32 v115, v115, v23
	v_add_f32_e32 v115, v115, v25
	v_fma_f32 v115, v115, s97, -v19
	v_add_f32_e32 v232, 0, v18
	v_add_f32_e32 v232, v232, v19
	v_add_f32_e32 v232, v232, v21
	v_add_f32_e32 v232, v232, v23
	v_fma_f32 v232, v232, s97, -v18
	v_cvt_pk_bf16_f32 v115, v115, v232
	ds_write_b16 v0, v115 offset:47840
	ds_write_b16_d16_hi v0, v115 offset:48880
	v_add_f32_e32 v115, 0, v16
	v_add_f32_e32 v115, v115, v18
	v_add_f32_e32 v115, v115, v19
	v_add_f32_e32 v115, v115, v21
	v_fma_f32 v115, v115, s97, -v16
	v_add_f32_e32 v232, 0, v14
	v_add_f32_e32 v232, v232, v16
	v_add_f32_e32 v232, v232, v18
	v_add_f32_e32 v232, v232, v19
	v_fma_f32 v232, v232, s97, -v14
	v_cvt_pk_bf16_f32 v115, v115, v232
	ds_write_b16 v0, v115 offset:49920
	ds_write_b16_d16_hi v0, v115 offset:50960
	v_add_f32_e32 v115, 0, v12
	v_add_f32_e32 v115, v115, v14
	v_add_f32_e32 v115, v115, v16
	v_add_f32_e32 v115, v115, v18
	v_fma_f32 v115, v115, s97, -v12
	v_add_f32_e32 v232, 0, v9
	v_add_f32_e32 v232, v232, v12
	v_add_f32_e32 v232, v232, v14
	v_add_f32_e32 v232, v232, v16
	v_fma_f32 v232, v232, s97, -v9
	v_cvt_pk_bf16_f32 v115, v115, v232
	ds_write_b16 v0, v115 offset:52000
	ds_write_b16_d16_hi v0, v115 offset:53040
	v_add_f32_e32 v115, 0, v7
	v_add_f32_e32 v115, v115, v9
	v_add_f32_e32 v115, v115, v12
	v_add_f32_e32 v115, v115, v14
	v_fma_f32 v115, v115, s97, -v7
	v_add_f32_e32 v232, 0, v5
	v_add_f32_e32 v232, v232, v7
	v_add_f32_e32 v232, v232, v9
	v_add_f32_e32 v232, v232, v12
	v_fma_f32 v232, v232, s97, -v5
	v_cvt_pk_bf16_f32 v115, v115, v232
	ds_write_b16 v0, v115 offset:54080
	ds_write_b16_d16_hi v0, v115 offset:55120
	v_add_f32_e32 v115, 0, v3
	v_add_f32_e32 v115, v115, v5
	v_add_f32_e32 v115, v115, v7
	v_add_f32_e32 v115, v115, v9
	v_fma_f32 v115, v115, s97, -v3
	v_add_f32_e32 v232, 0, v17
	v_add_f32_e32 v232, v232, v3
	v_add_f32_e32 v232, v232, v5
	v_add_f32_e32 v232, v232, v7
	v_fma_f32 v232, v232, s97, -v17
	v_cvt_pk_bf16_f32 v115, v115, v232
	ds_write_b16 v0, v115 offset:56160
	ds_write_b16_d16_hi v0, v115 offset:57200
	v_add_f32_e32 v115, 0, v15
	v_add_f32_e32 v115, v115, v17
	v_add_f32_e32 v115, v115, v3
	v_add_f32_e32 v115, v115, v5
	v_fma_f32 v115, v115, s97, -v15
	v_add_f32_e32 v232, 0, v13
	v_add_f32_e32 v232, v232, v15
	v_add_f32_e32 v232, v232, v17
	v_add_f32_e32 v232, v232, v3
	v_fma_f32 v232, v232, s97, -v13
	v_cvt_pk_bf16_f32 v115, v115, v232
	ds_write_b16 v0, v115 offset:58240
	ds_write_b16_d16_hi v0, v115 offset:59280
	v_add_f32_e32 v115, 0, v11
	v_add_f32_e32 v115, v115, v13
	v_add_f32_e32 v115, v115, v15
	v_add_f32_e32 v115, v115, v17
	v_fma_f32 v115, v115, s97, -v11
	v_add_f32_e32 v232, 0, v10
	v_add_f32_e32 v232, v232, v11
	v_add_f32_e32 v232, v232, v13
	v_add_f32_e32 v232, v232, v15
	v_fma_f32 v232, v232, s97, -v10
	v_cvt_pk_bf16_f32 v115, v115, v232
	ds_write_b16 v0, v115 offset:60320
	ds_write_b16_d16_hi v0, v115 offset:61360
	v_add_f32_e32 v115, 0, v8
	v_add_f32_e32 v115, v115, v10
	v_add_f32_e32 v115, v115, v11
	v_add_f32_e32 v115, v115, v13
	v_fma_f32 v115, v115, s97, -v8
	v_add_f32_e32 v232, 0, v6
	v_add_f32_e32 v232, v232, v8
	v_add_f32_e32 v232, v232, v10
	v_add_f32_e32 v232, v232, v11
	v_fma_f32 v232, v232, s97, -v6
	v_cvt_pk_bf16_f32 v115, v115, v232
	ds_write_b16 v0, v115 offset:62400
	ds_write_b16_d16_hi v0, v115 offset:63440
	v_add_f32_e32 v115, 0, v4
	v_add_f32_e32 v115, v115, v6
	v_add_f32_e32 v115, v115, v8
	v_add_f32_e32 v115, v115, v10
	v_fma_f32 v115, v115, s97, -v4
	v_cvt_pk_bf16_f32 v115, v115, s0
	ds_write_b16 v0, v115 offset:64480
	v_add_f32_e32 v115, 0, v2
	v_add_f32_e32 v115, v115, v4
	v_add_f32_e32 v115, v115, v6
	v_add_f32_e32 v115, v115, v8
	v_mul_f32_e32 v137, 0x3e800000, v115

.LBB0_595:
	s_and_b64 vcc, exec, s[8:9]
	s_cbranch_vccz .LBB0_597
	v_cndmask_b32_e64 v115, 0.5, 1.0, s[6:7]
	v_fma_f32 v114, v115, v114, -v49
	v_cvt_pk_bf16_f32 v114, v114, s0
	ds_write_b16 v0, v114
	v_add_f32_e32 v114, 0, v46
	v_add_f32_e32 v49, v114, v49
	v_fma_f32 v49, v49, 0.5, -v46
	v_cvt_pk_bf16_f32 v49, v49, s0
	ds_write_b16 v0, v49 offset:1040
	v_add_f32_e32 v49, 0, v43
	v_add_f32_e32 v46, v49, v46
	v_fma_f32 v46, v46, 0.5, -v43
	v_cvt_pk_bf16_f32 v46, v46, s0
	ds_write_b16 v0, v46 offset:2080
	v_add_f32_e32 v46, 0, v41
	v_add_f32_e32 v43, v46, v43
	v_fma_f32 v43, v43, 0.5, -v41
	v_cvt_pk_bf16_f32 v43, v43, s0
	ds_write_b16 v0, v43 offset:3120
	v_add_f32_e32 v43, 0, v38
	v_add_f32_e32 v41, v43, v41
	v_fma_f32 v41, v41, 0.5, -v38
	v_cvt_pk_bf16_f32 v41, v41, s0
	ds_write_b16 v0, v41 offset:4160
	v_add_f32_e32 v41, 0, v35
	v_add_f32_e32 v38, v41, v38
	v_fma_f32 v38, v38, 0.5, -v35
	v_cvt_pk_bf16_f32 v38, v38, s0
	ds_write_b16 v0, v38 offset:5200
	v_add_f32_e32 v38, 0, v32
	v_add_f32_e32 v35, v38, v35
	v_fma_f32 v35, v35, 0.5, -v32
	v_cvt_pk_bf16_f32 v35, v35, s0
	ds_write_b16 v0, v35 offset:6240
	v_add_f32_e32 v35, 0, v39
	v_add_f32_e32 v32, v35, v32
	v_fma_f32 v32, v32, 0.5, -v39
	v_add_f32_e32 v232, 0, v36
	v_add_f32_e32 v232, v232, v39
	v_fma_f32 v232, v232, 0.5, -v36
	v_cvt_pk_bf16_f32 v32, v32, v232
	ds_write_b16 v0, v32 offset:7280
	ds_write_b16_d16_hi v0, v32 offset:8320
	v_add_f32_e32 v32, 0, v33
	v_add_f32_e32 v32, v32, v36
	v_fma_f32 v32, v32, 0.5, -v33
	v_add_f32_e32 v232, 0, v29
	v_add_f32_e32 v232, v232, v33
	v_fma_f32 v232, v232, 0.5, -v29
	v_cvt_pk_bf16_f32 v32, v32, v232
	ds_write_b16 v0, v32 offset:9360
	ds_write_b16_d16_hi v0, v32 offset:10400
	v_add_f32_e32 v32, 0, v26
	v_add_f32_e32 v29, v32, v29
	v_fma_f32 v29, v29, 0.5, -v26
	v_cvt_pk_bf16_f32 v29, v29, s0
	ds_write_b16 v0, v29 offset:11440
	v_add_f32_e32 v29, 0, v24
	v_add_f32_e32 v26, v29, v26
	v_fma_f32 v26, v26, 0.5, -v24
	v_cvt_pk_bf16_f32 v26, v26, s0
	ds_write_b16 v0, v26 offset:12480
	v_add_f32_e32 v26, 0, v22
	v_add_f32_e32 v24, v26, v24
	v_fma_f32 v24, v24, 0.5, -v22
	v_cvt_pk_bf16_f32 v24, v24, s0
	ds_write_b16 v0, v24 offset:13520
	v_add_f32_e32 v24, 0, v20
	v_add_f32_e32 v22, v24, v22
	v_fma_f32 v22, v22, 0.5, -v20
	v_cvt_pk_bf16_f32 v22, v22, s0
	ds_write_b16 v0, v22 offset:14560
	v_add_f32_e32 v22, 0, v64
	v_add_f32_e32 v20, v22, v20
	v_fma_f32 v20, v20, 0.5, -v64
	v_add_f32_e32 v232, 0, v62
	v_add_f32_e32 v232, v232, v64
	v_fma_f32 v232, v232, 0.5, -v62
	v_cvt_pk_bf16_f32 v20, v20, v232
	ds_write_b16 v0, v20 offset:15600
	ds_write_b16_d16_hi v0, v20 offset:16640
	v_add_f32_e32 v20, 0, v65
	v_add_f32_e32 v20, v20, v62
	v_fma_f32 v20, v20, 0.5, -v65
	v_add_f32_e32 v232, 0, v63
	v_add_f32_e32 v232, v232, v65
	v_fma_f32 v232, v232, 0.5, -v63
	v_cvt_pk_bf16_f32 v20, v20, v232
	ds_write_b16 v0, v20 offset:17680
	ds_write_b16_d16_hi v0, v20 offset:18720
	v_add_f32_e32 v20, 0, v61
	v_add_f32_e32 v20, v20, v63
	v_fma_f32 v20, v20, 0.5, -v61
	v_add_f32_e32 v232, 0, v60
	v_add_f32_e32 v232, v232, v61
	v_fma_f32 v232, v232, 0.5, -v60
	v_cvt_pk_bf16_f32 v20, v20, v232
	ds_write_b16 v0, v20 offset:19760
	ds_write_b16_d16_hi v0, v20 offset:20800
	v_add_f32_e32 v20, 0, v59
	v_add_f32_e32 v20, v20, v60
	v_fma_f32 v20, v20, 0.5, -v59
	v_add_f32_e32 v232, 0, v58
	v_add_f32_e32 v232, v232, v59
	v_fma_f32 v232, v232, 0.5, -v58
	v_cvt_pk_bf16_f32 v20, v20, v232
	ds_write_b16 v0, v20 offset:21840
	ds_write_b16_d16_hi v0, v20 offset:22880
	v_add_f32_e32 v20, 0, v56
	v_add_f32_e32 v20, v20, v58
	v_fma_f32 v20, v20, 0.5, -v56
	v_add_f32_e32 v232, 0, v54
	v_add_f32_e32 v232, v232, v56
	v_fma_f32 v232, v232, 0.5, -v54
	v_cvt_pk_bf16_f32 v20, v20, v232
	ds_write_b16 v0, v20 offset:23920
	ds_write_b16_d16_hi v0, v20 offset:24960
	v_add_f32_e32 v20, 0, v57
	v_add_f32_e32 v20, v20, v54
	v_fma_f32 v20, v20, 0.5, -v57
	v_add_f32_e32 v232, 0, v55
	v_add_f32_e32 v232, v232, v57
	v_fma_f32 v232, v232, 0.5, -v55
	v_cvt_pk_bf16_f32 v20, v20, v232
	ds_write_b16 v0, v20 offset:26000
	ds_write_b16_d16_hi v0, v20 offset:27040
	v_add_f32_e32 v20, 0, v53
	v_add_f32_e32 v20, v20, v55
	v_fma_f32 v20, v20, 0.5, -v53
	v_add_f32_e32 v232, 0, v52
	v_add_f32_e32 v232, v232, v53
	v_fma_f32 v232, v232, 0.5, -v52
	v_cvt_pk_bf16_f32 v20, v20, v232
	ds_write_b16 v0, v20 offset:28080
	ds_write_b16_d16_hi v0, v20 offset:29120
	v_add_f32_e32 v20, 0, v51
	v_add_f32_e32 v20, v20, v52
	v_fma_f32 v20, v20, 0.5, -v51
	v_add_f32_e32 v232, 0, v50
	v_add_f32_e32 v232, v232, v51
	v_fma_f32 v232, v232, 0.5, -v50
	v_cvt_pk_bf16_f32 v20, v20, v232
	ds_write_b16 v0, v20 offset:30160
	ds_write_b16_d16_hi v0, v20 offset:31200
	v_add_f32_e32 v20, 0, v47
	v_add_f32_e32 v20, v20, v50
	v_fma_f32 v20, v20, 0.5, -v47
	v_add_f32_e32 v232, 0, v44
	v_add_f32_e32 v232, v232, v47
	v_fma_f32 v232, v232, 0.5, -v44
	v_cvt_pk_bf16_f32 v20, v20, v232
	ds_write_b16 v0, v20 offset:32240
	ds_write_b16_d16_hi v0, v20 offset:33280
	v_add_f32_e32 v20, 0, v48
	v_add_f32_e32 v20, v20, v44
	v_fma_f32 v20, v20, 0.5, -v48
	v_add_f32_e32 v232, 0, v45
	v_add_f32_e32 v232, v232, v48
	v_fma_f32 v232, v232, 0.5, -v45
	v_cvt_pk_bf16_f32 v20, v20, v232
	ds_write_b16 v0, v20 offset:34320
	ds_write_b16_d16_hi v0, v20 offset:35360
	v_add_f32_e32 v20, 0, v42
	v_add_f32_e32 v20, v20, v45
	v_fma_f32 v20, v20, 0.5, -v42
	v_add_f32_e32 v232, 0, v40
	v_add_f32_e32 v232, v232, v42
	v_fma_f32 v232, v232, 0.5, -v40
	v_cvt_pk_bf16_f32 v20, v20, v232
	ds_write_b16 v0, v20 offset:36400
	ds_write_b16_d16_hi v0, v20 offset:37440
	v_add_f32_e32 v20, 0, v37
	v_add_f32_e32 v20, v20, v40
	v_fma_f32 v20, v20, 0.5, -v37
	v_add_f32_e32 v232, 0, v34
	v_add_f32_e32 v232, v232, v37
	v_fma_f32 v232, v232, 0.5, -v34
	v_cvt_pk_bf16_f32 v20, v20, v232
	ds_write_b16 v0, v20 offset:38480
	ds_write_b16_d16_hi v0, v20 offset:39520
	v_add_f32_e32 v20, 0, v30
	v_add_f32_e32 v20, v20, v34
	v_fma_f32 v20, v20, 0.5, -v30
	v_add_f32_e32 v232, 0, v27
	v_add_f32_e32 v232, v232, v30
	v_fma_f32 v232, v232, 0.5, -v27
	v_cvt_pk_bf16_f32 v20, v20, v232
	ds_write_b16 v0, v20 offset:40560
	ds_write_b16_d16_hi v0, v20 offset:41600
	v_add_f32_e32 v20, 0, v31
	v_add_f32_e32 v20, v20, v27
	v_fma_f32 v20, v20, 0.5, -v31
	v_add_f32_e32 v232, 0, v28
	v_add_f32_e32 v232, v232, v31
	v_fma_f32 v232, v232, 0.5, -v28
	v_cvt_pk_bf16_f32 v20, v20, v232
	ds_write_b16 v0, v20 offset:42640
	ds_write_b16_d16_hi v0, v20 offset:43680
	v_add_f32_e32 v20, 0, v25
	v_add_f32_e32 v20, v20, v28
	v_fma_f32 v20, v20, 0.5, -v25
	v_add_f32_e32 v232, 0, v23
	v_add_f32_e32 v232, v232, v25
	v_fma_f32 v232, v232, 0.5, -v23
	v_cvt_pk_bf16_f32 v20, v20, v232
	ds_write_b16 v0, v20 offset:44720
	ds_write_b16_d16_hi v0, v20 offset:45760
	v_add_f32_e32 v20, 0, v21
	v_add_f32_e32 v20, v20, v23
	v_fma_f32 v20, v20, 0.5, -v21
	v_add_f32_e32 v232, 0, v19
	v_add_f32_e32 v232, v232, v21
	v_fma_f32 v232, v232, 0.5, -v19
	v_cvt_pk_bf16_f32 v20, v20, v232
	ds_write_b16 v0, v20 offset:46800
	ds_write_b16_d16_hi v0, v20 offset:47840
	v_add_f32_e32 v20, 0, v18
	v_add_f32_e32 v19, v20, v19
	v_fma_f32 v19, v19, 0.5, -v18
	v_cvt_pk_bf16_f32 v19, v19, s0
	ds_write_b16 v0, v19 offset:48880
	v_add_f32_e32 v19, 0, v16
	v_add_f32_e32 v18, v19, v18
	v_fma_f32 v18, v18, 0.5, -v16
	v_cvt_pk_bf16_f32 v18, v18, s0
	ds_write_b16 v0, v18 offset:49920
	v_add_f32_e32 v18, 0, v14
	v_add_f32_e32 v16, v18, v16
	v_fma_f32 v16, v16, 0.5, -v14
	v_cvt_pk_bf16_f32 v16, v16, s0
	ds_write_b16 v0, v16 offset:50960
	v_add_f32_e32 v16, 0, v12
	v_add_f32_e32 v14, v16, v14
	v_fma_f32 v14, v14, 0.5, -v12
	v_cvt_pk_bf16_f32 v14, v14, s0
	ds_write_b16 v0, v14 offset:52000
	v_add_f32_e32 v14, 0, v9
	v_add_f32_e32 v12, v14, v12
	v_fma_f32 v12, v12, 0.5, -v9
	v_cvt_pk_bf16_f32 v12, v12, s0
	ds_write_b16 v0, v12 offset:53040
	v_add_f32_e32 v12, 0, v7
	v_add_f32_e32 v9, v12, v9
	v_fma_f32 v9, v9, 0.5, -v7
	v_cvt_pk_bf16_f32 v9, v9, s0
	ds_write_b16 v0, v9 offset:54080
	v_add_f32_e32 v9, 0, v5
	v_add_f32_e32 v7, v9, v7
	v_fma_f32 v7, v7, 0.5, -v5
	v_cvt_pk_bf16_f32 v7, v7, s0
	ds_write_b16 v0, v7 offset:55120
	v_add_f32_e32 v7, 0, v3
	v_add_f32_e32 v5, v7, v5
	v_fma_f32 v5, v5, 0.5, -v3
	v_cvt_pk_bf16_f32 v5, v5, s0
	ds_write_b16 v0, v5 offset:56160
	v_add_f32_e32 v5, 0, v17
	v_add_f32_e32 v3, v5, v3
	v_fma_f32 v3, v3, 0.5, -v17
	v_add_f32_e32 v232, 0, v15
	v_add_f32_e32 v232, v232, v17
	v_fma_f32 v232, v232, 0.5, -v15
	v_cvt_pk_bf16_f32 v3, v3, v232
	ds_write_b16 v0, v3 offset:57200
	ds_write_b16_d16_hi v0, v3 offset:58240
	v_add_f32_e32 v3, 0, v13
	v_add_f32_e32 v3, v3, v15
	v_fma_f32 v3, v3, 0.5, -v13
	v_add_f32_e32 v232, 0, v11
	v_add_f32_e32 v232, v232, v13
	v_fma_f32 v232, v232, 0.5, -v11
	v_cvt_pk_bf16_f32 v3, v3, v232
	ds_write_b16 v0, v3 offset:59280
	ds_write_b16_d16_hi v0, v3 offset:60320
	v_add_f32_e32 v3, 0, v10
	v_add_f32_e32 v3, v3, v11
	v_fma_f32 v3, v3, 0.5, -v10
	v_add_f32_e32 v232, 0, v8
	v_add_f32_e32 v232, v232, v10
	v_fma_f32 v232, v232, 0.5, -v8
	v_cvt_pk_bf16_f32 v3, v3, v232
	ds_write_b16 v0, v3 offset:61360
	ds_write_b16_d16_hi v0, v3 offset:62400
	v_add_f32_e32 v3, 0, v6
	v_add_f32_e32 v3, v3, v8
	v_fma_f32 v3, v3, 0.5, -v6
	v_add_f32_e32 v232, 0, v4
	v_add_f32_e32 v232, v232, v6
	v_fma_f32 v232, v232, 0.5, -v4
	v_cvt_pk_bf16_f32 v3, v3, v232
	ds_write_b16 v0, v3 offset:63440
	ds_write_b16_d16_hi v0, v3 offset:64480
	v_add_f32_e32 v3, 0, v2
	v_add_f32_e32 v3, v3, v4
	v_mul_f32_e32 v137, 0.5, v3
.LBB0_597:
	v_sub_f32_e32 v2, v137, v2
	v_cvt_pk_bf16_f32 v2, v2, s0
	s_mov_b64 s[4:5], s[0:1]
	ds_write_b16 v0, v2 offset:65520
	s_waitcnt lgkmcnt(0)
	s_barrier
	s_waitcnt vmcnt(0)
	s_load_dwordx2 s[8:9], s[4:5], 0xd0
	s_nop 0
	s_load_dwordx2 s[4:5], s[4:5], 0x68
	v_mbcnt_lo_u32_b32 v0, -1, 0
	v_mbcnt_hi_u32_b32 v0, -1, v0
	s_add_i32 s34, s34, s46
	v_add_u32_e32 v0, s67, v0
	s_waitcnt lgkmcnt(0)
	s_add_u32 s6, s4, s38
	v_readfirstlane_b32 s4, v0
	s_addc_u32 s7, s5, s39
	v_and_b32_e32 v164, 31, v234
	v_or_b32_e32 v164, s67, v164
	v_ashrrev_i32_e32 v165, 31, v164
	v_lshl_add_u64 v[164:165], v[164:165], 2, s[6:7]
	global_load_dword v166, v[164:165], off
	global_load_dword v167, v[164:165], off offset:128
	s_ashr_i32 s10, s4, 7
	s_ashr_i32 s11, s10, 31
	s_and_b32 s5, s4, 64
	s_lshl_b64 s[10:11], s[10:11], 7
	v_and_b32_e32 v123, 31, v0
	s_or_b32 s5, s10, s5
	v_or_b32_e32 v2, s5, v123
	v_mov_b32_e32 v3, s11
	v_bfe_u32 v122, v0, 5, 1
	v_lshlrev_b64 v[2:3], 8, v[2:3]
	v_lshl_add_u64 v[2:3], s[8:9], 0, v[2:3]
	v_lshlrev_b32_e32 v0, 4, v122
	v_lshl_add_u64 v[6:7], v[2:3], 0, v[0:1]
	s_mov_b32 s5, 0x1600000
	v_add_co_u32_e32 v2, vcc, s5, v6
	s_mov_b64 s[8:9], 0x1600000
	s_nop 0
	v_addc_co_u32_e32 v3, vcc, 0, v7, vcc

	v_lshl_add_u64 v[114:115], v[6:7], 0, s[8:9]
	s_mov_b64 s[8:9], 0x1602000
	s_mov_b32 s5, 0x1602000
	v_lshl_add_u64 v[156:157], v[6:7], 0, s[8:9]
	v_add_co_u32_e32 v6, vcc, s5, v6
	s_lshl_b32 s5, s4, 1
	s_nop 0
	v_addc_co_u32_e32 v7, vcc, 0, v7, vcc

	s_nop 0


	s_and_b32 s5, s5, 0xffffff00
	v_mul_u32_u24_e32 v10, 0x410, v123
	v_or_b32_e32 v0, s5, v0
	v_add3_u32 v0, 0, v10, v0
	ds_read_b128 v[10:13], v0 offset:33280
	ds_read_b128 v[14:17], v0
	ds_read_b128 v[148:151], v0 offset:32
	ds_read_b128 v[152:155], v0 offset:33312
	s_andn2_b32 s4, s4, 63
	v_mul_u32_u24_e32 v122, 0x1040, v122
	s_cmpk_gt_i32 s34, 0x1ff
	s_waitcnt vmcnt(6) lgkmcnt(2)
	v_mfma_f32_32x32x16_bf16 v[18:33], v[14:17], v[172:175], 0
	v_mfma_f32_32x32x16_bf16 v[50:65], v[14:17], v[168:171], 0
	v_mfma_f32_32x32x16_bf16 v[34:49], v[10:13], v[168:171], 0
	v_mfma_f32_32x32x16_bf16 v[2:17], v[10:13], v[172:175], 0
	s_waitcnt vmcnt(5) lgkmcnt(1)
	v_mfma_f32_32x32x16_bf16 v[50:65], v[148:151], v[176:179], v[50:65]
	s_waitcnt vmcnt(4)
	v_mfma_f32_32x32x16_bf16 v[18:33], v[148:151], v[180:183], v[18:33]
	s_waitcnt lgkmcnt(0)
	v_mfma_f32_32x32x16_bf16 v[34:49], v[152:155], v[176:179], v[34:49]
	v_mfma_f32_32x32x16_bf16 v[2:17], v[152:155], v[180:183], v[2:17]
	ds_read_b128 v[124:127], v0 offset:64
	ds_read_b128 v[128:131], v0 offset:33344
	s_waitcnt vmcnt(3) lgkmcnt(1)
	v_mfma_f32_32x32x16_bf16 v[50:65], v[124:127], v[184:187], v[50:65]
	s_waitcnt vmcnt(2)
	v_mfma_f32_32x32x16_bf16 v[18:33], v[124:127], v[188:191], v[18:33]
	s_waitcnt lgkmcnt(0)
	v_mfma_f32_32x32x16_bf16 v[34:49], v[128:131], v[184:187], v[34:49]
	v_mfma_f32_32x32x16_bf16 v[2:17], v[128:131], v[188:191], v[2:17]
	ds_read_b128 v[124:127], v0 offset:96
	ds_read_b128 v[128:131], v0 offset:33376
	s_waitcnt vmcnt(1) lgkmcnt(1)
	v_mfma_f32_32x32x16_bf16 v[50:65], v[124:127], v[192:195], v[50:65]
	s_waitcnt vmcnt(0)
	v_mfma_f32_32x32x16_bf16 v[18:33], v[124:127], v[196:199], v[18:33]
	s_waitcnt lgkmcnt(0)
	v_mfma_f32_32x32x16_bf16 v[34:49], v[128:131], v[192:195], v[34:49]
	v_mfma_f32_32x32x16_bf16 v[2:17], v[128:131], v[196:199], v[2:17]


	ds_read_b128 v[156:159], v0 offset:128
	ds_read_b128 v[160:163], v0 offset:33408
	s_waitcnt vmcnt(7) lgkmcnt(1)
	v_mfma_f32_32x32x16_bf16 v[50:65], v[156:159], v[200:203], v[50:65]
	s_waitcnt vmcnt(6)
	v_mfma_f32_32x32x16_bf16 v[18:33], v[156:159], v[204:207], v[18:33]
	s_waitcnt lgkmcnt(0)
	v_mfma_f32_32x32x16_bf16 v[34:49], v[160:163], v[200:203], v[34:49]
	v_mfma_f32_32x32x16_bf16 v[2:17], v[160:163], v[204:207], v[2:17]
	ds_read_b128 v[124:127], v0 offset:160
	ds_read_b128 v[128:131], v0 offset:33440
	s_waitcnt vmcnt(5) lgkmcnt(1)
	v_mfma_f32_32x32x16_bf16 v[50:65], v[124:127], v[208:211], v[50:65]
	s_waitcnt vmcnt(4)
	v_mfma_f32_32x32x16_bf16 v[18:33], v[124:127], v[212:215], v[18:33]
	s_waitcnt lgkmcnt(0)
	v_mfma_f32_32x32x16_bf16 v[34:49], v[128:131], v[208:211], v[34:49]
	v_mfma_f32_32x32x16_bf16 v[2:17], v[128:131], v[212:215], v[2:17]
	ds_read_b128 v[124:127], v0 offset:192
	ds_read_b128 v[128:131], v0 offset:33472
	s_waitcnt vmcnt(3) lgkmcnt(1)
	v_mfma_f32_32x32x16_bf16 v[50:65], v[124:127], v[216:219], v[50:65]
	s_waitcnt vmcnt(2)
	v_mfma_f32_32x32x16_bf16 v[18:33], v[124:127], v[220:223], v[18:33]
	s_waitcnt lgkmcnt(0)
	v_mfma_f32_32x32x16_bf16 v[34:49], v[128:131], v[216:219], v[34:49]
	v_mfma_f32_32x32x16_bf16 v[2:17], v[128:131], v[220:223], v[2:17]
	ds_read_b128 v[124:127], v0 offset:224
	ds_read_b128 v[128:131], v0 offset:33504
	s_waitcnt lgkmcnt(0)
	s_barrier
	s_waitcnt vmcnt(1)
	v_mfma_f32_32x32x16_bf16 v[50:65], v[124:127], v[224:227], v[50:65]
	s_waitcnt vmcnt(0)
	v_mfma_f32_32x32x16_bf16 v[18:33], v[124:127], v[228:231], v[18:33]
	v_or_b32_e32 v124, s4, v123
	v_ashrrev_i32_e32 v125, 31, v124
	v_lshl_add_u64 v[114:115], v[124:125], 2, s[6:7]
	v_mov_b32_e32 v123, v166
	v_lshlrev_b32_e32 v0, 1, v124
	v_add3_u32 v0, 0, v0, v122
	s_waitcnt vmcnt(0)
	s_nop 2
	v_mul_f32_e32 v50, v50, v123
	v_mfma_f32_32x32x16_bf16 v[34:49], v[128:131], v[224:227], v[34:49]
	v_mul_f32_e32 v232, v51, v123
	v_cvt_pk_bf16_f32 v50, v50, v232
	ds_write_b16 v0, v50
	ds_write_b16_d16_hi v0, v50 offset:1040
	v_mul_f32_e32 v50, v52, v123
	s_nop 4
	v_mul_f32_e32 v34, v34, v123
	v_mul_f32_e32 v232, v35, v123
	v_cvt_pk_bf16_f32 v34, v34, v232
	ds_write_b16 v0, v34 offset:33280
	ds_write_b16_d16_hi v0, v34 offset:34320
	v_mul_f32_e32 v34, v36, v123
	v_mul_f32_e32 v232, v37, v123
	v_cvt_pk_bf16_f32 v34, v34, v232
	ds_write_b16 v0, v34 offset:35360
	ds_write_b16_d16_hi v0, v34 offset:36400
	v_mul_f32_e32 v34, v38, v123
	v_mul_f32_e32 v232, v39, v123
	v_cvt_pk_bf16_f32 v34, v34, v232
	ds_write_b16 v0, v34 offset:41600
	ds_write_b16_d16_hi v0, v34 offset:42640
	v_mul_f32_e32 v34, v40, v123
	v_mul_f32_e32 v232, v41, v123
	v_cvt_pk_bf16_f32 v34, v34, v232
	ds_write_b16 v0, v34 offset:43680
	ds_write_b16_d16_hi v0, v34 offset:44720
	v_mul_f32_e32 v34, v42, v123
	v_mul_f32_e32 v232, v43, v123
	v_cvt_pk_bf16_f32 v34, v34, v232
	ds_write_b16 v0, v34 offset:49920
	ds_write_b16_d16_hi v0, v34 offset:50960
	v_mul_f32_e32 v34, v44, v123
	v_mul_f32_e32 v232, v45, v123
	v_cvt_pk_bf16_f32 v34, v34, v232
	ds_write_b16 v0, v34 offset:52000
	ds_write_b16_d16_hi v0, v34 offset:53040
	v_mul_f32_e32 v34, v46, v123
	v_mul_f32_e32 v232, v47, v123
	v_cvt_pk_bf16_f32 v34, v34, v232
	ds_write_b16 v0, v34 offset:58240
	ds_write_b16_d16_hi v0, v34 offset:59280
	v_mul_f32_e32 v34, v48, v123
	v_mul_f32_e32 v232, v49, v123
	v_cvt_pk_bf16_f32 v34, v34, v232
	ds_write_b16 v0, v34 offset:60320
	ds_write_b16_d16_hi v0, v34 offset:61360
	v_mov_b32_e32 v34, v167
	v_mfma_f32_32x32x16_bf16 v[2:17], v[128:131], v[228:231], v[2:17]
	v_mul_f32_e32 v232, v53, v123
	v_cvt_pk_bf16_f32 v50, v50, v232
	ds_write_b16 v0, v50 offset:2080
	ds_write_b16_d16_hi v0, v50 offset:3120
	v_mul_f32_e32 v50, v54, v123
	v_mul_f32_e32 v232, v55, v123
	v_cvt_pk_bf16_f32 v50, v50, v232
	ds_write_b16 v0, v50 offset:8320
	ds_write_b16_d16_hi v0, v50 offset:9360
	v_mul_f32_e32 v50, v56, v123
	v_mul_f32_e32 v232, v57, v123
	v_cvt_pk_bf16_f32 v50, v50, v232
	ds_write_b16 v0, v50 offset:10400
	ds_write_b16_d16_hi v0, v50 offset:11440
	v_mul_f32_e32 v50, v58, v123
	v_mul_f32_e32 v232, v59, v123
	v_cvt_pk_bf16_f32 v50, v50, v232
	ds_write_b16 v0, v50 offset:16640
	ds_write_b16_d16_hi v0, v50 offset:17680
	v_mul_f32_e32 v50, v60, v123
	v_mul_f32_e32 v232, v61, v123
	v_cvt_pk_bf16_f32 v50, v50, v232
	ds_write_b16 v0, v50 offset:18720
	ds_write_b16_d16_hi v0, v50 offset:19760
	v_mul_f32_e32 v50, v62, v123
	v_mul_f32_e32 v232, v63, v123
	v_cvt_pk_bf16_f32 v50, v50, v232
	ds_write_b16 v0, v50 offset:24960
	ds_write_b16_d16_hi v0, v50 offset:26000
	v_mul_f32_e32 v50, v64, v123
	v_mul_f32_e32 v232, v65, v123
	v_cvt_pk_bf16_f32 v50, v50, v232
	ds_write_b16 v0, v50 offset:27040
	ds_write_b16_d16_hi v0, v50 offset:28080
	s_waitcnt vmcnt(0)
	v_mul_f32_e32 v18, v18, v34
	v_mul_f32_e32 v2, v2, v34
	v_cvt_pk_bf16_f32 v18, v18, s0
	v_cvt_pk_bf16_f32 v2, v2, s0
	ds_write_b16 v0, v18 offset:64
	v_mul_f32_e32 v18, v19, v34
	ds_write_b16 v0, v2 offset:33344
	v_mul_f32_e32 v2, v3, v34
	v_cvt_pk_bf16_f32 v18, v18, s0
	v_cvt_pk_bf16_f32 v2, v2, s0
	ds_write_b16 v0, v18 offset:1104
	v_mul_f32_e32 v18, v20, v34
	ds_write_b16 v0, v2 offset:34384
	v_mul_f32_e32 v2, v4, v34
	v_cvt_pk_bf16_f32 v18, v18, s0
	v_cvt_pk_bf16_f32 v2, v2, s0
	ds_write_b16 v0, v18 offset:2144
	v_mul_f32_e32 v18, v21, v34
	ds_write_b16 v0, v2 offset:35424
	v_mul_f32_e32 v2, v5, v34
	v_cvt_pk_bf16_f32 v18, v18, s0
	v_cvt_pk_bf16_f32 v2, v2, s0
	ds_write_b16 v0, v18 offset:3184
	v_mul_f32_e32 v18, v22, v34
	ds_write_b16 v0, v2 offset:36464
	v_mul_f32_e32 v2, v6, v34
	v_cvt_pk_bf16_f32 v18, v18, s0
	v_cvt_pk_bf16_f32 v2, v2, s0
	ds_write_b16 v0, v18 offset:8384
	v_mul_f32_e32 v18, v23, v34
	ds_write_b16 v0, v2 offset:41664
	v_mul_f32_e32 v2, v7, v34
	v_cvt_pk_bf16_f32 v18, v18, s0
	v_cvt_pk_bf16_f32 v2, v2, s0
	ds_write_b16 v0, v18 offset:9424
	v_mul_f32_e32 v18, v24, v34
	ds_write_b16 v0, v2 offset:42704
	v_mul_f32_e32 v2, v8, v34
	v_cvt_pk_bf16_f32 v18, v18, s0
	v_cvt_pk_bf16_f32 v2, v2, s0
	ds_write_b16 v0, v18 offset:10464
	v_mul_f32_e32 v18, v25, v34
	ds_write_b16 v0, v2 offset:43744
	v_mul_f32_e32 v2, v9, v34
	v_cvt_pk_bf16_f32 v18, v18, s0
	v_cvt_pk_bf16_f32 v2, v2, s0
	ds_write_b16 v0, v18 offset:11504
	v_mul_f32_e32 v18, v26, v34
	ds_write_b16 v0, v2 offset:44784
	v_mul_f32_e32 v2, v10, v34
	v_cvt_pk_bf16_f32 v18, v18, s0
	v_cvt_pk_bf16_f32 v2, v2, s0
	ds_write_b16 v0, v18 offset:16704
	v_mul_f32_e32 v18, v27, v34
	ds_write_b16 v0, v2 offset:49984
	v_mul_f32_e32 v2, v11, v34
	v_cvt_pk_bf16_f32 v18, v18, s0
	v_cvt_pk_bf16_f32 v2, v2, s0
	ds_write_b16 v0, v18 offset:17744
	v_mul_f32_e32 v18, v28, v34
	ds_write_b16 v0, v2 offset:51024
	v_mul_f32_e32 v2, v12, v34
	v_cvt_pk_bf16_f32 v18, v18, s0
	v_cvt_pk_bf16_f32 v2, v2, s0
	ds_write_b16 v0, v18 offset:18784
	v_mul_f32_e32 v18, v29, v34
	ds_write_b16 v0, v2 offset:52064
	v_mul_f32_e32 v2, v13, v34
	v_cvt_pk_bf16_f32 v18, v18, s0
	v_cvt_pk_bf16_f32 v2, v2, s0
	ds_write_b16 v0, v18 offset:19824
	v_mul_f32_e32 v18, v30, v34
	ds_write_b16 v0, v2 offset:53104
	v_mul_f32_e32 v2, v14, v34
	v_cvt_pk_bf16_f32 v18, v18, s0
	v_cvt_pk_bf16_f32 v2, v2, s0
	ds_write_b16 v0, v18 offset:25024
	v_mul_f32_e32 v18, v31, v34
	ds_write_b16 v0, v2 offset:58304
	v_mul_f32_e32 v2, v15, v34
	v_cvt_pk_bf16_f32 v18, v18, s0
	v_cvt_pk_bf16_f32 v2, v2, s0
	ds_write_b16 v0, v18 offset:26064
	v_mul_f32_e32 v18, v32, v34
	ds_write_b16 v0, v2 offset:59344
	v_mul_f32_e32 v2, v16, v34
	v_cvt_pk_bf16_f32 v18, v18, s0
	v_cvt_pk_bf16_f32 v2, v2, s0
	ds_write_b16 v0, v18 offset:27104
	v_mul_f32_e32 v18, v33, v34
	ds_write_b16 v0, v2 offset:60384
	v_mul_f32_e32 v2, v17, v34
	v_cvt_pk_bf16_f32 v18, v18, s0
	v_cvt_pk_bf16_f32 v2, v2, s0
	ds_write_b16 v0, v18 offset:28144
	ds_write_b16 v0, v2 offset:61424
	s_waitcnt lgkmcnt(0)
	s_barrier
	s_cbranch_scc1 .LBB0_599
	s_mov_b64 s[4:5], s[0:1]
	s_load_dwordx2 s[4:5], s[4:5], 0xd0
	s_bfe_i32 s9, s34, 0x10019
	v_mbcnt_lo_u32_b32 v0, -1, 0
	v_mbcnt_hi_u32_b32 v0, -1, v0
	s_lshl_b32 s8, s34, 6
	v_add_u32_e32 v8, s67, v0
	s_lshr_b32 s9, s9, 21
	s_add_i32 s9, s8, s9
	v_lshlrev_b32_e32 v0, 4, v8
	s_and_b32 s9, s9, 0xfffff800
	v_and_b32_e32 v0, 0x3f0, v0
	s_sub_i32 s8, s9, s8
	s_waitcnt lgkmcnt(0)
	v_lshl_add_u64 v[2:3], s[4:5], 0, v[0:1]
	v_min_i32_e32 v0, 0x177f, v8
	s_or_b32 s8, s8, 30
	v_ashrrev_i32_e32 v0, 6, v0
	s_ashr_i32 s35, s34, 31
	v_max_i32_e32 v4, s8, v0
	v_min_i32_e32 v0, 0x157f, v8
	s_lshl_b64 s[6:7], s[34:35], 6
	v_add_u32_e32 v0, 0x200, v0
	s_add_u32 s6, s6, 0xffffffe2
	v_ashrrev_i32_e32 v0, 6, v0
	s_addc_u32 s7, s7, -1
	v_ashrrev_i32_e32 v5, 31, v4
	v_max_i32_e32 v6, s8, v0
	s_mov_b64 s[4:5], 0xfc00000
	v_lshl_add_u64 v[4:5], s[6:7], 0, v[4:5]
	v_ashrrev_i32_e32 v7, 31, v6
	v_min_i32_e32 v0, 0x137f, v8
	v_lshl_add_u64 v[2:3], v[2:3], 0, s[4:5]
	v_lshlrev_b64 v[4:5], 10, v[4:5]
	v_lshl_add_u64 v[6:7], s[6:7], 0, v[6:7]
	v_add_u32_e32 v0, 0x400, v0
	v_lshl_add_u64 v[4:5], v[2:3], 0, v[4:5]
	v_lshlrev_b64 v[6:7], 10, v[6:7]
	v_ashrrev_i32_e32 v0, 6, v0
	v_lshl_add_u64 v[6:7], v[2:3], 0, v[6:7]
	global_load_dwordx4 v[66:69], v[4:5], off
	global_load_dwordx4 v[70:73], v[6:7], off
	v_max_i32_e32 v4, s8, v0
	v_min_i32_e32 v0, 0x117f, v8
	v_add_u32_e32 v0, 0x600, v0
	v_ashrrev_i32_e32 v0, 6, v0
	v_ashrrev_i32_e32 v5, 31, v4
	v_max_i32_e32 v6, s8, v0
	v_lshl_add_u64 v[4:5], s[6:7], 0, v[4:5]
	v_ashrrev_i32_e32 v7, 31, v6
	v_min_i32_e32 v0, 0xf7f, v8
	v_lshlrev_b64 v[4:5], 10, v[4:5]
	v_lshl_add_u64 v[6:7], s[6:7], 0, v[6:7]
	v_add_u32_e32 v0, 0x800, v0
	v_lshl_add_u64 v[4:5], v[2:3], 0, v[4:5]
	v_lshlrev_b64 v[6:7], 10, v[6:7]
	v_ashrrev_i32_e32 v0, 6, v0
	v_lshl_add_u64 v[6:7], v[2:3], 0, v[6:7]
	global_load_dwordx4 v[74:77], v[4:5], off
	global_load_dwordx4 v[78:81], v[6:7], off
	v_max_i32_e32 v4, s8, v0
	v_min_i32_e32 v0, 0xd7f, v8
	v_add_u32_e32 v0, 0xa00, v0
	v_ashrrev_i32_e32 v0, 6, v0
	v_ashrrev_i32_e32 v5, 31, v4
	v_max_i32_e32 v6, s8, v0
	v_lshl_add_u64 v[4:5], s[6:7], 0, v[4:5]
	v_ashrrev_i32_e32 v7, 31, v6
	v_min_i32_e32 v0, 0xb7f, v8
	v_lshlrev_b64 v[4:5], 10, v[4:5]
	v_lshl_add_u64 v[6:7], s[6:7], 0, v[6:7]
	v_add_u32_e32 v0, 0xc00, v0
	v_lshl_add_u64 v[4:5], v[2:3], 0, v[4:5]
	v_lshlrev_b64 v[6:7], 10, v[6:7]
	v_ashrrev_i32_e32 v0, 6, v0
	v_lshl_add_u64 v[6:7], v[2:3], 0, v[6:7]
	global_load_dwordx4 v[82:85], v[4:5], off
	global_load_dwordx4 v[86:89], v[6:7], off
	v_max_i32_e32 v4, s8, v0
	v_min_i32_e32 v0, 0x97f, v8
	v_add_u32_e32 v0, 0xe00, v0
	v_ashrrev_i32_e32 v0, 6, v0
	v_ashrrev_i32_e32 v5, 31, v4
	v_max_i32_e32 v6, s8, v0
	v_lshl_add_u64 v[4:5], s[6:7], 0, v[4:5]
	v_ashrrev_i32_e32 v7, 31, v6
	v_min_i32_e32 v0, 0x77f, v8
	v_lshlrev_b64 v[4:5], 10, v[4:5]
	v_lshl_add_u64 v[6:7], s[6:7], 0, v[6:7]
	v_add_u32_e32 v0, 0x1000, v0
	v_lshl_add_u64 v[4:5], v[2:3], 0, v[4:5]
	v_lshlrev_b64 v[6:7], 10, v[6:7]
	v_ashrrev_i32_e32 v0, 6, v0
	v_lshl_add_u64 v[6:7], v[2:3], 0, v[6:7]
	global_load_dwordx4 v[90:93], v[4:5], off
	global_load_dwordx4 v[94:97], v[6:7], off
	v_max_i32_e32 v4, s8, v0
	v_min_i32_e32 v0, 0x57f, v8
	v_add_u32_e32 v0, 0x1200, v0
	v_ashrrev_i32_e32 v0, 6, v0
	v_ashrrev_i32_e32 v5, 31, v4
	v_max_i32_e32 v6, s8, v0
	v_lshl_add_u64 v[4:5], s[6:7], 0, v[4:5]
	v_ashrrev_i32_e32 v7, 31, v6
	v_min_i32_e32 v0, 0x37f, v8
	v_lshlrev_b64 v[4:5], 10, v[4:5]
	v_lshl_add_u64 v[6:7], s[6:7], 0, v[6:7]
	v_add_u32_e32 v0, 0x1400, v0
	v_lshl_add_u64 v[4:5], v[2:3], 0, v[4:5]
	v_lshlrev_b64 v[6:7], 10, v[6:7]
	v_ashrrev_i32_e32 v0, 6, v0
	v_lshl_add_u64 v[6:7], v[2:3], 0, v[6:7]
	global_load_dwordx4 v[98:101], v[4:5], off
	global_load_dwordx4 v[102:105], v[6:7], off
	v_max_i32_e32 v4, s8, v0
	v_min_i32_e32 v0, 0x17f, v8
	v_add_u32_e32 v0, 0x1600, v0
	v_ashrrev_i32_e32 v0, 6, v0
	v_ashrrev_i32_e32 v5, 31, v4
	v_max_i32_e32 v6, s8, v0
	v_lshl_add_u64 v[4:5], s[6:7], 0, v[4:5]
	v_ashrrev_i32_e32 v7, 31, v6
	v_lshlrev_b64 v[4:5], 10, v[4:5]
	v_lshl_add_u64 v[6:7], s[6:7], 0, v[6:7]
	v_lshl_add_u64 v[4:5], v[2:3], 0, v[4:5]
	v_lshlrev_b64 v[6:7], 10, v[6:7]
	v_lshl_add_u64 v[2:3], v[2:3], 0, v[6:7]
	global_load_dwordx4 v[106:109], v[4:5], off
	global_load_dwordx4 v[110:113], v[2:3], off
